# P0: w_up/w_down converted by a workgroup-cooperative 128x128 transposer (x4 loads, full-line fp8 stores, double-buffered); attention QK^T K-fragment reads software-pipelined
# speedup vs baseline: 1.0098x; 1.0098x over previous
; #define GAS __attribute__((address_space(1)))
;     const int pr = item >> 1, kb = 2 * (pr / nblk) + (item & 1), nb = pr % nblk, k0 = 64 * kb, n0 = 32 * nb;
;     const int nr = n0 + (lane & 31); const int sc = MAP == 1 ? src_col_in(nr) : nr;
;     float v[32];
; #pragma unroll
;     for (int i = 0; i < 32; ++i) v[i] = sc >= 0 ? W[(size_t)(k0 + 2 * i + (lane >> 5)) * Nsrc + sc] : 0.f;
; #pragma unroll
;     for (int i = 0; i < 32; ++i) { const int k = k0 + 2 * i + (lane >> 5); float x = v[i] * wscale; if (KS) x *= (k < ksplit ? ksA[k] : ksB[k - ksplit]); scr[(2 * i + (lane >> 5)) * 33 + (lane & 31)] = x; }
;     LDS_WAIT(); asm volatile("" ::: "memory");
;     const int c = lane & 7;
; #pragma unroll
;     for (int j = 0; j < 4; ++j) { const int n = (lane >> 3) + 8 * j; const LAS float* s = scr + (8 * c) * 33 + n;
;         const unsigned long long o = (unsigned long long)pg8::pk4_fp8(s[0 * 33], s[1 * 33], s[2 * 33], s[3 * 33]) | ((unsigned long long)pg8::pk4_fp8(s[4 * 33], s[5 * 33], s[6 * 33], s[7 * 33]) << 32);
;         *(GAS unsigned long long*)(WT + (size_t)(n0 + n) * K + k0 + 8 * c) = o; }
;     LDS_WAIT(); asm volatile("" ::: "memory");
; }
; __global__ void __launch_bounds__(NWAVES * 64, 2) hybrid_fwd(Args args) {
;     ...
;         for (int rep = 0; rep < REP_PRO; ++rep)
;         for (int it = gw; it < DEPTH * I_L; it += NGW) {
;             const int l = it / I_L; int r = it % I_L;
;             if (r < I_IN) { if (l >= PROJ_F8_FROM) p0_transpose_item_f8<true, 1>(args.in[2] + (size_t)l * DM * NSRC, DM, NSRC, NPROJ / 32, (unsigned char*)(ws + WS_WIN + l * SZ_WIN), WUP8_SCALE, args.in[1] + l * DM, args.in[1] + l * DM, DM, scr, r, lane);
;                 else p0_transpose_item<1, true>(args.in[2] + (size_t)l * DM * NSRC, DM, NSRC, NPROJ / 32, (bf16*)(ws + WS_WIN + l * SZ_WIN), args.in[1] + l * DM, args.in[1] + l * DM, DM, scr, r, lane); continue; } r -= I_IN;
;             if (r < I_O) { if (l >= WO_F8_FROM) p0_transpose_item_f8<true>(args.in[13] + (size_t)l * DM * DM, DM, DM, DM / 32, (unsigned char*)(ws + WS_WO + l * SZ_WO), 64.f, args.in[6] + l * 2048, args.in[12] + l * 2048, 2048, scr, r, lane);
;                 else p0_transpose_item<0, true>(args.in[13] + (size_t)l * DM * DM, DM, DM, DM / 32, (bf16*)(ws + WS_WO + l * SZ_WO), args.in[6] + l * 2048, args.in[12] + l * 2048, 2048, scr, r, lane); continue; } r -= I_O;
.LBB0_11:
	s_or_b64 exec, exec, s[0:1]
	v_mov_b32_e32 v1, v0
	v_readlane_b32 s1, v253, 2
	v_readfirstlane_b32 s0, v1
	s_ashr_i32 s0, s0, 6
	s_lshl_b32 s1, s1, 3
	s_add_i32 s80, s0, s1
	s_lshl_b32 s0, s0, 14
	v_lshlrev_b32_e32 v2, 3, v1
	v_writelane_b32 v253, s1, 46
	s_add_i32 s1, s0, 0
	v_and_b32_e32 v18, 31, v1
	v_bfe_u32 v20, v1, 3, 3
	v_and_b32_e32 v8, 56, v2
	s_lshl_b32 s96, s83, 3
	s_lshl_b32 s76, s83, 9
	v_bfe_u32 v6, v1, 5, 1
	v_lshl_add_u32 v25, v18, 2, s1
	s_movk_i32 s0, 0x84
	v_mul_u32_u24_e32 v2, 0x84, v8
	v_lshlrev_b32_e32 v3, 2, v20
	s_cmp_gt_i32 s80, 0x2f3ff
	v_mad_u32_u24 v19, v6, s0, v25
	v_mov_b32_e32 v11, 0
	v_add3_u32 v21, s1, v2, v3
	v_or_b32_e32 v22, 8, v20
	v_or_b32_e32 v23, 16, v20
	v_or_b32_e32 v24, 24, v20
	s_cbranch_scc1 .LBB0_192
	v_and_b32_e32 v249, 63, v0
	v_lshrrev_b32_e32 v250, 6, v0
	v_readlane_b32 s15, v253, 2
	v_lshrrev_b32_e32 v246, 5, v249
	v_lshl_add_u32 v247, v250, 4, v246
	v_and_b32_e32 v248, 31, v249
	v_xor_b32_e32 v248, v248, v250
	v_lshlrev_b32_e32 v248, 4, v248
	v_lshl_add_u32 v209, v247, 9, v248
	v_add_u32_e32 v210, 0x10000, v209
	v_lshlrev_b32_e32 v217, 2, v247
	v_and_b32_e32 v246, 7, v249
	v_lshrrev_b32_e32 v247, 5, v249
	v_lshl_add_u32 v247, v250, 2, v247
	v_xor_b32_e32 v247, v247, v246
	v_lshlrev_b32_e32 v247, 4, v247
	v_lshl_add_u32 v247, v246, 13, v247
	v_bfe_u32 v248, v249, 3, 2
	v_lshl_add_u32 v211, v248, 2, v247
	v_add_u32_e32 v212, 0x10000, v211
	v_and_b32_e32 v246, 7, v249
	v_lshrrev_b32_e32 v247, 5, v249
	v_lshl_add_u32 v247, v250, 2, v247
	v_add_u32_e32 v247, 2, v247
	v_xor_b32_e32 v247, v247, v246
	v_lshlrev_b32_e32 v247, 4, v247
	v_lshl_add_u32 v247, v246, 13, v247
	v_bfe_u32 v248, v249, 3, 2
	v_lshl_add_u32 v213, v248, 2, v247
	v_add_u32_e32 v214, 0x10000, v213
	v_lshrrev_b32_e32 v246, 5, v249
	v_lshl_add_u32 v246, v250, 4, v246
	v_and_b32_e32 v247, 31, v249
	v_lshlrev_b32_e32 v247, 4, v247
	v_lshl_add_u32 v208, v246, 16, v247
	v_lshrrev_b32_e32 v246, 3, v249
	v_lshl_add_u32 v246, v250, 4, v246
	v_and_b32_e32 v247, 7, v249
	v_lshlrev_b32_e32 v247, 4, v247
	v_lshl_add_u32 v215, v246, 12, v247
	v_add_u32_e32 v216, 0x8000, v215
	s_lshr_b32 s22, s15, 3
	s_and_b32 s23, s15, 7
	v_readlane_b32 s16, v253, 33
	v_readlane_b32 s17, v253, 34
	v_readlane_b32 s18, v253, 41
	v_readlane_b32 s19, v253, 42
	s_lshl_b32 s20, s22, 23
	s_lshl_b32 s21, s23, 9
	s_add_u32 s20, s20, s21
	s_add_u32 s16, s16, s20
	s_addc_u32 s17, s17, 0
	s_add_u32 s18, s18, 0xf600000
	s_addc_u32 s19, s19, 0
	s_lshl_b32 s20, s23, 19
	s_lshl_b32 s21, s22, 7
	s_add_u32 s20, s20, s21
	s_add_u32 s18, s18, s20
	s_addc_u32 s19, s19, 0
	v_readlane_b32 s10, v253, 31
	v_readlane_b32 s11, v253, 32
	s_lshl_b32 s20, s22, 9
	s_add_u32 s10, s10, s20
	s_addc_u32 s11, s11, 0
	s_mov_b32 s13, 0
.Lco_wup_layer:
	s_mov_b64 s[4:5], s[16:17]
	s_mov_b64 s[6:7], s[18:19]
	s_mov_b32 s24, 0
	s_mov_b32 s25, 0
	s_mov_b32 s44, 0xc3e00000
	v_mov_b32_e32 v246, 0x43e00000
	global_load_dword v218, v217, s[10:11] offset:0
	global_load_dword v219, v217, s[10:11] offset:8
	global_load_dword v220, v217, s[10:11] offset:16
	global_load_dword v221, v217, s[10:11] offset:24
	global_load_dword v222, v217, s[10:11] offset:32
	global_load_dword v223, v217, s[10:11] offset:40
	global_load_dword v224, v217, s[10:11] offset:48
	global_load_dword v225, v217, s[10:11] offset:56
	s_waitcnt vmcnt(0)
	v_mul_f32_e32 v218, 0x42800000, v218
	v_mul_f32_e32 v219, 0x42800000, v219
	v_mul_f32_e32 v220, 0x42800000, v220
	v_mul_f32_e32 v221, 0x42800000, v221
	v_mul_f32_e32 v222, 0x42800000, v222
	v_mul_f32_e32 v223, 0x42800000, v223
	v_mul_f32_e32 v224, 0x42800000, v224
	v_mul_f32_e32 v225, 0x42800000, v225
	s_mov_b64 s[8:9], s[4:5]
	global_load_dwordx4 v[144:147], v208, s[8:9]
	s_add_u32 s8, s8, 0x20000
	s_addc_u32 s9, s9, 0
	global_load_dwordx4 v[148:151], v208, s[8:9]
	s_add_u32 s8, s8, 0x20000
	s_addc_u32 s9, s9, 0
	global_load_dwordx4 v[152:155], v208, s[8:9]
	s_add_u32 s8, s8, 0x20000
	s_addc_u32 s9, s9, 0
	global_load_dwordx4 v[156:159], v208, s[8:9]
	s_add_u32 s8, s8, 0x20000
	s_addc_u32 s9, s9, 0
	global_load_dwordx4 v[160:163], v208, s[8:9]
	s_add_u32 s8, s8, 0x20000
	s_addc_u32 s9, s9, 0
	global_load_dwordx4 v[164:167], v208, s[8:9]
	s_add_u32 s8, s8, 0x20000
	s_addc_u32 s9, s9, 0
	global_load_dwordx4 v[168:171], v208, s[8:9]
	s_add_u32 s8, s8, 0x20000
	s_addc_u32 s9, s9, 0
	global_load_dwordx4 v[172:175], v208, s[8:9]
	s_add_u32 s4, s4, 0x1000
	s_addc_u32 s5, s5, 0
	s_mov_b64 s[8:9], s[4:5]
	global_load_dwordx4 v[176:179], v208, s[8:9]
	s_add_u32 s8, s8, 0x20000
	s_addc_u32 s9, s9, 0
	global_load_dwordx4 v[180:183], v208, s[8:9]
	s_add_u32 s8, s8, 0x20000
	s_addc_u32 s9, s9, 0
	global_load_dwordx4 v[184:187], v208, s[8:9]
	s_add_u32 s8, s8, 0x20000
	s_addc_u32 s9, s9, 0
	global_load_dwordx4 v[188:191], v208, s[8:9]
	s_add_u32 s8, s8, 0x20000
	s_addc_u32 s9, s9, 0
	global_load_dwordx4 v[192:195], v208, s[8:9]
	s_add_u32 s8, s8, 0x20000
	s_addc_u32 s9, s9, 0
	global_load_dwordx4 v[196:199], v208, s[8:9]
	s_add_u32 s8, s8, 0x20000
	s_addc_u32 s9, s9, 0
	global_load_dwordx4 v[200:203], v208, s[8:9]
	s_add_u32 s8, s8, 0x20000
	s_addc_u32 s9, s9, 0
	global_load_dwordx4 v[204:207], v208, s[8:9]
	s_add_u32 s4, s4, 0x1000
	s_addc_u32 s5, s5, 0
	s_waitcnt vmcnt(8)
	v_mul_f32_e32 v144, v218, v144
	v_mul_f32_e32 v145, v218, v145
	v_mul_f32_e32 v146, v218, v146
	v_mul_f32_e32 v147, v218, v147
	ds_write_b128 v209, v[144:147]
	v_mul_f32_e32 v148, v219, v148
	v_mul_f32_e32 v149, v219, v149
	v_mul_f32_e32 v150, v219, v150
	v_mul_f32_e32 v151, v219, v151
	ds_write_b128 v209, v[148:151] offset:1024
	v_mul_f32_e32 v152, v220, v152
	v_mul_f32_e32 v153, v220, v153
	v_mul_f32_e32 v154, v220, v154
	v_mul_f32_e32 v155, v220, v155
	ds_write_b128 v209, v[152:155] offset:2048
	v_mul_f32_e32 v156, v221, v156
	v_mul_f32_e32 v157, v221, v157
	v_mul_f32_e32 v158, v221, v158
	v_mul_f32_e32 v159, v221, v159
	ds_write_b128 v209, v[156:159] offset:3072
	v_mul_f32_e32 v160, v222, v160
	v_mul_f32_e32 v161, v222, v161
	v_mul_f32_e32 v162, v222, v162
	v_mul_f32_e32 v163, v222, v163
	ds_write_b128 v209, v[160:163] offset:4096
	v_mul_f32_e32 v164, v223, v164
	v_mul_f32_e32 v165, v223, v165
	v_mul_f32_e32 v166, v223, v166
	v_mul_f32_e32 v167, v223, v167
	ds_write_b128 v209, v[164:167] offset:5120
	v_mul_f32_e32 v168, v224, v168
	v_mul_f32_e32 v169, v224, v169
	v_mul_f32_e32 v170, v224, v170
	v_mul_f32_e32 v171, v224, v171
	ds_write_b128 v209, v[168:171] offset:6144
	v_mul_f32_e32 v172, v225, v172
	v_mul_f32_e32 v173, v225, v173
	v_mul_f32_e32 v174, v225, v174
	v_mul_f32_e32 v175, v225, v175
	ds_write_b128 v209, v[172:175] offset:7168
	s_waitcnt lgkmcnt(0)
	s_barrier
; #define GAS __attribute__((address_space(1)))
; #define LAS __attribute__((address_space(3)))
; #define LDS_WAIT() asm volatile("s_waitcnt lgkmcnt(0)" ::: "memory")
;     const int pr = item >> 1, kb = 2 * (pr / nblk) + (item & 1), nb = pr % nblk, k0 = 64 * kb, n0 = 32 * nb;
;     const int nr = n0 + (lane & 31); const int sc = MAP == 1 ? src_col_in(nr) : nr;
;     float v[32];
; #pragma unroll
;     for (int i = 0; i < 32; ++i) v[i] = sc >= 0 ? W[(size_t)(k0 + 2 * i + (lane >> 5)) * Nsrc + sc] : 0.f;
; #pragma unroll
;     for (int i = 0; i < 32; ++i) { const int k = k0 + 2 * i + (lane >> 5); float x = v[i] * wscale; if (KS) x *= (k < ksplit ? ksA[k] : ksB[k - ksplit]); scr[(2 * i + (lane >> 5)) * 33 + (lane & 31)] = x; }
;     LDS_WAIT(); asm volatile("" ::: "memory");
;     const int c = lane & 7;
; #pragma unroll
;     for (int j = 0; j < 4; ++j) { const int n = (lane >> 3) + 8 * j; const LAS float* s = scr + (8 * c) * 33 + n;
;         const unsigned long long o = (unsigned long long)pg8::pk4_fp8(s[0 * 33], s[1 * 33], s[2 * 33], s[3 * 33]) | ((unsigned long long)pg8::pk4_fp8(s[4 * 33], s[5 * 33], s[6 * 33], s[7 * 33]) << 32);
;         *(GAS unsigned long long*)(WT + (size_t)(n0 + n) * K + k0 + 8 * c) = o; }
;     LDS_WAIT(); asm volatile("" ::: "memory");
; }
	s_mov_b64 s[8:9], s[4:5]
	global_load_dwordx4 v[144:147], v208, s[8:9]
	s_add_u32 s8, s8, 0x20000
	s_addc_u32 s9, s9, 0
	global_load_dwordx4 v[148:151], v208, s[8:9]
	s_add_u32 s8, s8, 0x20000
	s_addc_u32 s9, s9, 0
	global_load_dwordx4 v[152:155], v208, s[8:9]
	s_add_u32 s8, s8, 0x20000
	s_addc_u32 s9, s9, 0
	global_load_dwordx4 v[156:159], v208, s[8:9]
	s_add_u32 s8, s8, 0x20000
	s_addc_u32 s9, s9, 0
	global_load_dwordx4 v[160:163], v208, s[8:9]
	s_add_u32 s8, s8, 0x20000
	s_addc_u32 s9, s9, 0
	global_load_dwordx4 v[164:167], v208, s[8:9]
	s_add_u32 s8, s8, 0x20000
	s_addc_u32 s9, s9, 0
	global_load_dwordx4 v[168:171], v208, s[8:9]
	s_add_u32 s8, s8, 0x20000
	s_addc_u32 s9, s9, 0
	global_load_dwordx4 v[172:175], v208, s[8:9]
	s_add_u32 s4, s4, 0x1000
	s_addc_u32 s5, s5, 0
	ds_read_b32 v226, v211
	ds_read_b32 v227, v211 offset:512
	ds_read_b32 v228, v211 offset:1024
	ds_read_b32 v229, v211 offset:1536
	ds_read_b32 v230, v211 offset:2048
	ds_read_b32 v231, v211 offset:2560
	ds_read_b32 v232, v211 offset:3072
	ds_read_b32 v233, v211 offset:3584
	ds_read_b32 v234, v211 offset:4096
	ds_read_b32 v235, v211 offset:4608
	ds_read_b32 v236, v211 offset:5120
	ds_read_b32 v237, v211 offset:5632
	ds_read_b32 v238, v211 offset:6144
	ds_read_b32 v239, v211 offset:6656
	ds_read_b32 v240, v211 offset:7168
	ds_read_b32 v241, v211 offset:7680
	s_waitcnt lgkmcnt(0)
	v_max_f32_e32 v226, v226, v226
	v_max_f32_e32 v227, v227, v227
	v_max_f32_e32 v228, v228, v228
	v_max_f32_e32 v229, v229, v229
	v_max_f32_e32 v230, v230, v230
	v_max_f32_e32 v231, v231, v231
	v_max_f32_e32 v232, v232, v232
	v_max_f32_e32 v233, v233, v233
	v_max_f32_e32 v234, v234, v234
	v_max_f32_e32 v235, v235, v235
	v_max_f32_e32 v236, v236, v236
	v_max_f32_e32 v237, v237, v237
	v_max_f32_e32 v238, v238, v238
	v_max_f32_e32 v239, v239, v239
	v_max_f32_e32 v240, v240, v240
	v_max_f32_e32 v241, v241, v241
	v_med3_f32 v226, v226, s44, v246
	v_med3_f32 v227, v227, s44, v246
	v_med3_f32 v228, v228, s44, v246
	v_med3_f32 v229, v229, s44, v246
	v_med3_f32 v230, v230, s44, v246
	v_med3_f32 v231, v231, s44, v246
	v_med3_f32 v232, v232, s44, v246
	v_med3_f32 v233, v233, s44, v246
	v_med3_f32 v234, v234, s44, v246
	v_med3_f32 v235, v235, s44, v246
	v_med3_f32 v236, v236, s44, v246
	v_med3_f32 v237, v237, s44, v246
	v_med3_f32 v238, v238, s44, v246
	v_med3_f32 v239, v239, s44, v246
	v_med3_f32 v240, v240, s44, v246
	v_med3_f32 v241, v241, s44, v246
	v_mov_b32_e32 v242, 0
	v_mov_b32_e32 v243, 0
	v_mov_b32_e32 v244, 0
	v_mov_b32_e32 v245, 0
	v_cvt_pk_fp8_f32 v242, v226, v227
	v_cvt_pk_fp8_f32 v243, v230, v231
	v_cvt_pk_fp8_f32 v244, v234, v235
	v_cvt_pk_fp8_f32 v245, v238, v239
	v_cvt_pk_fp8_f32 v242, v228, v229 op_sel:[0,0,1]
	v_cvt_pk_fp8_f32 v243, v232, v233 op_sel:[0,0,1]
	v_cvt_pk_fp8_f32 v244, v236, v237 op_sel:[0,0,1]
	v_cvt_pk_fp8_f32 v245, v240, v241 op_sel:[0,0,1]
	s_nop 0
	global_store_dwordx4 v215, v[242:245], s[6:7]
	ds_read_b32 v226, v213
	ds_read_b32 v227, v213 offset:512
	ds_read_b32 v228, v213 offset:1024
	ds_read_b32 v229, v213 offset:1536
	ds_read_b32 v230, v213 offset:2048
	ds_read_b32 v231, v213 offset:2560
	ds_read_b32 v232, v213 offset:3072
	ds_read_b32 v233, v213 offset:3584
	ds_read_b32 v234, v213 offset:4096
	ds_read_b32 v235, v213 offset:4608
	ds_read_b32 v236, v213 offset:5120
	ds_read_b32 v237, v213 offset:5632
	ds_read_b32 v238, v213 offset:6144
	ds_read_b32 v239, v213 offset:6656
	ds_read_b32 v240, v213 offset:7168
	ds_read_b32 v241, v213 offset:7680
	s_waitcnt lgkmcnt(0)
	v_max_f32_e32 v226, v226, v226
	v_max_f32_e32 v227, v227, v227
	v_max_f32_e32 v228, v228, v228
	v_max_f32_e32 v229, v229, v229
	v_max_f32_e32 v230, v230, v230
	v_max_f32_e32 v231, v231, v231
	v_max_f32_e32 v232, v232, v232
	v_max_f32_e32 v233, v233, v233
	v_max_f32_e32 v234, v234, v234
	v_max_f32_e32 v235, v235, v235
	v_max_f32_e32 v236, v236, v236
	v_max_f32_e32 v237, v237, v237
	v_max_f32_e32 v238, v238, v238
	v_max_f32_e32 v239, v239, v239
	v_max_f32_e32 v240, v240, v240
	v_max_f32_e32 v241, v241, v241
	v_med3_f32 v226, v226, s44, v246
	v_med3_f32 v227, v227, s44, v246
	v_med3_f32 v228, v228, s44, v246
	v_med3_f32 v229, v229, s44, v246
	v_med3_f32 v230, v230, s44, v246
	v_med3_f32 v231, v231, s44, v246
	v_med3_f32 v232, v232, s44, v246
	v_med3_f32 v233, v233, s44, v246
	v_med3_f32 v234, v234, s44, v246
	v_med3_f32 v235, v235, s44, v246
	v_med3_f32 v236, v236, s44, v246
	v_med3_f32 v237, v237, s44, v246
	v_med3_f32 v238, v238, s44, v246
	v_med3_f32 v239, v239, s44, v246
	v_med3_f32 v240, v240, s44, v246
	v_med3_f32 v241, v241, s44, v246
	v_mov_b32_e32 v242, 0
	v_mov_b32_e32 v243, 0
	v_mov_b32_e32 v244, 0
	v_mov_b32_e32 v245, 0
	v_cvt_pk_fp8_f32 v242, v226, v227
	v_cvt_pk_fp8_f32 v243, v230, v231
	v_cvt_pk_fp8_f32 v244, v234, v235
	v_cvt_pk_fp8_f32 v245, v238, v239
	v_cvt_pk_fp8_f32 v242, v228, v229 op_sel:[0,0,1]
	v_cvt_pk_fp8_f32 v243, v232, v233 op_sel:[0,0,1]
	v_cvt_pk_fp8_f32 v244, v236, v237 op_sel:[0,0,1]
	v_cvt_pk_fp8_f32 v245, v240, v241 op_sel:[0,0,1]
	s_nop 0
	global_store_dwordx4 v216, v[242:245], s[6:7]
	s_add_u32 s6, s6, 0x400000
	s_addc_u32 s7, s7, 0
	s_waitcnt vmcnt(10)
	v_mul_f32_e32 v176, v218, v176
	v_mul_f32_e32 v177, v218, v177
	v_mul_f32_e32 v178, v218, v178
	v_mul_f32_e32 v179, v218, v179
	ds_write_b128 v210, v[176:179]
	v_mul_f32_e32 v180, v219, v180
	v_mul_f32_e32 v181, v219, v181
	v_mul_f32_e32 v182, v219, v182
	v_mul_f32_e32 v183, v219, v183
	ds_write_b128 v210, v[180:183] offset:1024
	v_mul_f32_e32 v184, v220, v184
	v_mul_f32_e32 v185, v220, v185
	v_mul_f32_e32 v186, v220, v186
	v_mul_f32_e32 v187, v220, v187
	ds_write_b128 v210, v[184:187] offset:2048
	v_mul_f32_e32 v188, v221, v188
	v_mul_f32_e32 v189, v221, v189
	v_mul_f32_e32 v190, v221, v190
	v_mul_f32_e32 v191, v221, v191
	ds_write_b128 v210, v[188:191] offset:3072
	v_mul_f32_e32 v192, v222, v192
	v_mul_f32_e32 v193, v222, v193
	v_mul_f32_e32 v194, v222, v194
	v_mul_f32_e32 v195, v222, v195
	ds_write_b128 v210, v[192:195] offset:4096
	v_mul_f32_e32 v196, v223, v196
	v_mul_f32_e32 v197, v223, v197
	v_mul_f32_e32 v198, v223, v198
	v_mul_f32_e32 v199, v223, v199
	ds_write_b128 v210, v[196:199] offset:5120
	v_mul_f32_e32 v200, v224, v200
	v_mul_f32_e32 v201, v224, v201
	v_mul_f32_e32 v202, v224, v202
	v_mul_f32_e32 v203, v224, v203
	ds_write_b128 v210, v[200:203] offset:6144
	v_mul_f32_e32 v204, v225, v204
	v_mul_f32_e32 v205, v225, v205
	v_mul_f32_e32 v206, v225, v206
	v_mul_f32_e32 v207, v225, v207
	ds_write_b128 v210, v[204:207] offset:7168
	s_waitcnt lgkmcnt(0)
	s_barrier
; #define GAS __attribute__((address_space(1)))
; #define LAS __attribute__((address_space(3)))
; #define LDS_WAIT() asm volatile("s_waitcnt lgkmcnt(0)" ::: "memory")
;     const int pr = item >> 1, kb = 2 * (pr / nblk) + (item & 1), nb = pr % nblk, k0 = 64 * kb, n0 = 32 * nb;
;     const int nr = n0 + (lane & 31); const int sc = MAP == 1 ? src_col_in(nr) : nr;
;     float v[32];
; #pragma unroll
;     for (int i = 0; i < 32; ++i) v[i] = sc >= 0 ? W[(size_t)(k0 + 2 * i + (lane >> 5)) * Nsrc + sc] : 0.f;
; #pragma unroll
;     for (int i = 0; i < 32; ++i) { const int k = k0 + 2 * i + (lane >> 5); float x = v[i] * wscale; if (KS) x *= (k < ksplit ? ksA[k] : ksB[k - ksplit]); scr[(2 * i + (lane >> 5)) * 33 + (lane & 31)] = x; }
;     LDS_WAIT(); asm volatile("" ::: "memory");
;     const int c = lane & 7;
; #pragma unroll
;     for (int j = 0; j < 4; ++j) { const int n = (lane >> 3) + 8 * j; const LAS float* s = scr + (8 * c) * 33 + n;
;         const unsigned long long o = (unsigned long long)pg8::pk4_fp8(s[0 * 33], s[1 * 33], s[2 * 33], s[3 * 33]) | ((unsigned long long)pg8::pk4_fp8(s[4 * 33], s[5 * 33], s[6 * 33], s[7 * 33]) << 32);
;         *(GAS unsigned long long*)(WT + (size_t)(n0 + n) * K + k0 + 8 * c) = o; }
;     LDS_WAIT(); asm volatile("" ::: "memory");
; }
	s_mov_b64 s[8:9], s[4:5]
	global_load_dwordx4 v[176:179], v208, s[8:9]
	s_add_u32 s8, s8, 0x20000
	s_addc_u32 s9, s9, 0
	global_load_dwordx4 v[180:183], v208, s[8:9]
	s_add_u32 s8, s8, 0x20000
	s_addc_u32 s9, s9, 0
	global_load_dwordx4 v[184:187], v208, s[8:9]
	s_add_u32 s8, s8, 0x20000
	s_addc_u32 s9, s9, 0
	global_load_dwordx4 v[188:191], v208, s[8:9]
	s_add_u32 s8, s8, 0x20000
	s_addc_u32 s9, s9, 0
	global_load_dwordx4 v[192:195], v208, s[8:9]
	s_add_u32 s8, s8, 0x20000
	s_addc_u32 s9, s9, 0
	global_load_dwordx4 v[196:199], v208, s[8:9]
	s_add_u32 s8, s8, 0x20000
	s_addc_u32 s9, s9, 0
	global_load_dwordx4 v[200:203], v208, s[8:9]
	s_add_u32 s8, s8, 0x20000
	s_addc_u32 s9, s9, 0
	global_load_dwordx4 v[204:207], v208, s[8:9]
	s_add_u32 s4, s4, 0x1000
	s_addc_u32 s5, s5, 0
	ds_read_b32 v226, v212
	ds_read_b32 v227, v212 offset:512
	ds_read_b32 v228, v212 offset:1024
	ds_read_b32 v229, v212 offset:1536
	ds_read_b32 v230, v212 offset:2048
	ds_read_b32 v231, v212 offset:2560
	ds_read_b32 v232, v212 offset:3072
	ds_read_b32 v233, v212 offset:3584
	ds_read_b32 v234, v212 offset:4096
	ds_read_b32 v235, v212 offset:4608
	ds_read_b32 v236, v212 offset:5120
	ds_read_b32 v237, v212 offset:5632
	ds_read_b32 v238, v212 offset:6144
	ds_read_b32 v239, v212 offset:6656
	ds_read_b32 v240, v212 offset:7168
	ds_read_b32 v241, v212 offset:7680
	s_waitcnt lgkmcnt(0)
	v_max_f32_e32 v226, v226, v226
	v_max_f32_e32 v227, v227, v227
	v_max_f32_e32 v228, v228, v228
	v_max_f32_e32 v229, v229, v229
	v_max_f32_e32 v230, v230, v230
	v_max_f32_e32 v231, v231, v231
	v_max_f32_e32 v232, v232, v232
	v_max_f32_e32 v233, v233, v233
	v_max_f32_e32 v234, v234, v234
	v_max_f32_e32 v235, v235, v235
	v_max_f32_e32 v236, v236, v236
	v_max_f32_e32 v237, v237, v237
	v_max_f32_e32 v238, v238, v238
	v_max_f32_e32 v239, v239, v239
	v_max_f32_e32 v240, v240, v240
	v_max_f32_e32 v241, v241, v241
	v_med3_f32 v226, v226, s44, v246
	v_med3_f32 v227, v227, s44, v246
	v_med3_f32 v228, v228, s44, v246
	v_med3_f32 v229, v229, s44, v246
	v_med3_f32 v230, v230, s44, v246
	v_med3_f32 v231, v231, s44, v246
	v_med3_f32 v232, v232, s44, v246
	v_med3_f32 v233, v233, s44, v246
	v_med3_f32 v234, v234, s44, v246
	v_med3_f32 v235, v235, s44, v246
	v_med3_f32 v236, v236, s44, v246
	v_med3_f32 v237, v237, s44, v246
	v_med3_f32 v238, v238, s44, v246
	v_med3_f32 v239, v239, s44, v246
	v_med3_f32 v240, v240, s44, v246
	v_med3_f32 v241, v241, s44, v246
	v_mov_b32_e32 v242, 0
	v_mov_b32_e32 v243, 0
	v_mov_b32_e32 v244, 0
	v_mov_b32_e32 v245, 0
	v_cvt_pk_fp8_f32 v242, v226, v227
	v_cvt_pk_fp8_f32 v243, v230, v231
	v_cvt_pk_fp8_f32 v244, v234, v235
	v_cvt_pk_fp8_f32 v245, v238, v239
	v_cvt_pk_fp8_f32 v242, v228, v229 op_sel:[0,0,1]
	v_cvt_pk_fp8_f32 v243, v232, v233 op_sel:[0,0,1]
	v_cvt_pk_fp8_f32 v244, v236, v237 op_sel:[0,0,1]
	v_cvt_pk_fp8_f32 v245, v240, v241 op_sel:[0,0,1]
	s_nop 0
	global_store_dwordx4 v215, v[242:245], s[6:7]
	ds_read_b32 v226, v214
	ds_read_b32 v227, v214 offset:512
	ds_read_b32 v228, v214 offset:1024
	ds_read_b32 v229, v214 offset:1536
	ds_read_b32 v230, v214 offset:2048
	ds_read_b32 v231, v214 offset:2560
	ds_read_b32 v232, v214 offset:3072
	ds_read_b32 v233, v214 offset:3584
	ds_read_b32 v234, v214 offset:4096
	ds_read_b32 v235, v214 offset:4608
	ds_read_b32 v236, v214 offset:5120
	ds_read_b32 v237, v214 offset:5632
	ds_read_b32 v238, v214 offset:6144
	ds_read_b32 v239, v214 offset:6656
	ds_read_b32 v240, v214 offset:7168
	ds_read_b32 v241, v214 offset:7680
	s_waitcnt lgkmcnt(0)
	v_max_f32_e32 v226, v226, v226
	v_max_f32_e32 v227, v227, v227
	v_max_f32_e32 v228, v228, v228
	v_max_f32_e32 v229, v229, v229
	v_max_f32_e32 v230, v230, v230
	v_max_f32_e32 v231, v231, v231
	v_max_f32_e32 v232, v232, v232
	v_max_f32_e32 v233, v233, v233
	v_max_f32_e32 v234, v234, v234
	v_max_f32_e32 v235, v235, v235
	v_max_f32_e32 v236, v236, v236
	v_max_f32_e32 v237, v237, v237
	v_max_f32_e32 v238, v238, v238
	v_max_f32_e32 v239, v239, v239
	v_max_f32_e32 v240, v240, v240
	v_max_f32_e32 v241, v241, v241
	v_med3_f32 v226, v226, s44, v246
	v_med3_f32 v227, v227, s44, v246
	v_med3_f32 v228, v228, s44, v246
	v_med3_f32 v229, v229, s44, v246
	v_med3_f32 v230, v230, s44, v246
	v_med3_f32 v231, v231, s44, v246
	v_med3_f32 v232, v232, s44, v246
	v_med3_f32 v233, v233, s44, v246
	v_med3_f32 v234, v234, s44, v246
	v_med3_f32 v235, v235, s44, v246
	v_med3_f32 v236, v236, s44, v246
	v_med3_f32 v237, v237, s44, v246
	v_med3_f32 v238, v238, s44, v246
	v_med3_f32 v239, v239, s44, v246
	v_med3_f32 v240, v240, s44, v246
	v_med3_f32 v241, v241, s44, v246
	v_mov_b32_e32 v242, 0
	v_mov_b32_e32 v243, 0
	v_mov_b32_e32 v244, 0
	v_mov_b32_e32 v245, 0
	v_cvt_pk_fp8_f32 v242, v226, v227
	v_cvt_pk_fp8_f32 v243, v230, v231
	v_cvt_pk_fp8_f32 v244, v234, v235
	v_cvt_pk_fp8_f32 v245, v238, v239
	v_cvt_pk_fp8_f32 v242, v228, v229 op_sel:[0,0,1]
	v_cvt_pk_fp8_f32 v243, v232, v233 op_sel:[0,0,1]
	v_cvt_pk_fp8_f32 v244, v236, v237 op_sel:[0,0,1]
	v_cvt_pk_fp8_f32 v245, v240, v241 op_sel:[0,0,1]
	s_nop 0
	global_store_dwordx4 v216, v[242:245], s[6:7]
	s_add_u32 s6, s6, 0x400000
	s_addc_u32 s7, s7, 0
	s_mov_b32 s12, 6
; #define GAS __attribute__((address_space(1)))
; #define LAS __attribute__((address_space(3)))
; #define LDS_WAIT() asm volatile("s_waitcnt lgkmcnt(0)" ::: "memory")
;     const int pr = item >> 1, kb = 2 * (pr / nblk) + (item & 1), nb = pr % nblk, k0 = 64 * kb, n0 = 32 * nb;
;     const int nr = n0 + (lane & 31); const int sc = MAP == 1 ? src_col_in(nr) : nr;
;     float v[32];
; #pragma unroll
;     for (int i = 0; i < 32; ++i) v[i] = sc >= 0 ? W[(size_t)(k0 + 2 * i + (lane >> 5)) * Nsrc + sc] : 0.f;
; #pragma unroll
;     for (int i = 0; i < 32; ++i) { const int k = k0 + 2 * i + (lane >> 5); float x = v[i] * wscale; if (KS) x *= (k < ksplit ? ksA[k] : ksB[k - ksplit]); scr[(2 * i + (lane >> 5)) * 33 + (lane & 31)] = x; }
;     LDS_WAIT(); asm volatile("" ::: "memory");
;     const int c = lane & 7;
; #pragma unroll
;     for (int j = 0; j < 4; ++j) { const int n = (lane >> 3) + 8 * j; const LAS float* s = scr + (8 * c) * 33 + n;
;         const unsigned long long o = (unsigned long long)pg8::pk4_fp8(s[0 * 33], s[1 * 33], s[2 * 33], s[3 * 33]) | ((unsigned long long)pg8::pk4_fp8(s[4 * 33], s[5 * 33], s[6 * 33], s[7 * 33]) << 32);
;         *(GAS unsigned long long*)(WT + (size_t)(n0 + n) * K + k0 + 8 * c) = o; }
;     LDS_WAIT(); asm volatile("" ::: "memory");
; }
.Lco_wup_loop:
	s_waitcnt vmcnt(12)
	v_mul_f32_e32 v144, v218, v144
	v_mul_f32_e32 v145, v218, v145
	v_mul_f32_e32 v146, v218, v146
	v_mul_f32_e32 v147, v218, v147
	ds_write_b128 v209, v[144:147]
	v_mul_f32_e32 v148, v219, v148
	v_mul_f32_e32 v149, v219, v149
	v_mul_f32_e32 v150, v219, v150
	v_mul_f32_e32 v151, v219, v151
	ds_write_b128 v209, v[148:151] offset:1024
	v_mul_f32_e32 v152, v220, v152
	v_mul_f32_e32 v153, v220, v153
	v_mul_f32_e32 v154, v220, v154
	v_mul_f32_e32 v155, v220, v155
	ds_write_b128 v209, v[152:155] offset:2048
	v_mul_f32_e32 v156, v221, v156
	v_mul_f32_e32 v157, v221, v157
	v_mul_f32_e32 v158, v221, v158
	v_mul_f32_e32 v159, v221, v159
	ds_write_b128 v209, v[156:159] offset:3072
	v_mul_f32_e32 v160, v222, v160
	v_mul_f32_e32 v161, v222, v161
	v_mul_f32_e32 v162, v222, v162
	v_mul_f32_e32 v163, v222, v163
	ds_write_b128 v209, v[160:163] offset:4096
	v_mul_f32_e32 v164, v223, v164
	v_mul_f32_e32 v165, v223, v165
	v_mul_f32_e32 v166, v223, v166
	v_mul_f32_e32 v167, v223, v167
	ds_write_b128 v209, v[164:167] offset:5120
	v_mul_f32_e32 v168, v224, v168
	v_mul_f32_e32 v169, v224, v169
	v_mul_f32_e32 v170, v224, v170
	v_mul_f32_e32 v171, v224, v171
	ds_write_b128 v209, v[168:171] offset:6144
	v_mul_f32_e32 v172, v225, v172
	v_mul_f32_e32 v173, v225, v173
	v_mul_f32_e32 v174, v225, v174
	v_mul_f32_e32 v175, v225, v175
	ds_write_b128 v209, v[172:175] offset:7168
	s_waitcnt lgkmcnt(0)
	s_barrier
	s_mov_b64 s[8:9], s[4:5]
	global_load_dwordx4 v[144:147], v208, s[8:9]
	s_add_u32 s8, s8, 0x20000
	s_addc_u32 s9, s9, 0
	global_load_dwordx4 v[148:151], v208, s[8:9]
	s_add_u32 s8, s8, 0x20000
	s_addc_u32 s9, s9, 0
	global_load_dwordx4 v[152:155], v208, s[8:9]
	s_add_u32 s8, s8, 0x20000
	s_addc_u32 s9, s9, 0
	global_load_dwordx4 v[156:159], v208, s[8:9]
	s_add_u32 s8, s8, 0x20000
	s_addc_u32 s9, s9, 0
	global_load_dwordx4 v[160:163], v208, s[8:9]
	s_add_u32 s8, s8, 0x20000
	s_addc_u32 s9, s9, 0
	global_load_dwordx4 v[164:167], v208, s[8:9]
	s_add_u32 s8, s8, 0x20000
	s_addc_u32 s9, s9, 0
	global_load_dwordx4 v[168:171], v208, s[8:9]
	s_add_u32 s8, s8, 0x20000
	s_addc_u32 s9, s9, 0
	global_load_dwordx4 v[172:175], v208, s[8:9]
	s_add_u32 s4, s4, 0x1000
	s_addc_u32 s5, s5, 0
	ds_read_b32 v226, v211
	ds_read_b32 v227, v211 offset:512
	ds_read_b32 v228, v211 offset:1024
	ds_read_b32 v229, v211 offset:1536
	ds_read_b32 v230, v211 offset:2048
	ds_read_b32 v231, v211 offset:2560
	ds_read_b32 v232, v211 offset:3072
	ds_read_b32 v233, v211 offset:3584
	ds_read_b32 v234, v211 offset:4096
	ds_read_b32 v235, v211 offset:4608
	ds_read_b32 v236, v211 offset:5120
	ds_read_b32 v237, v211 offset:5632
	ds_read_b32 v238, v211 offset:6144
	ds_read_b32 v239, v211 offset:6656
	ds_read_b32 v240, v211 offset:7168
	ds_read_b32 v241, v211 offset:7680
	s_waitcnt lgkmcnt(0)
	v_max_f32_e32 v226, v226, v226
	v_max_f32_e32 v227, v227, v227
	v_max_f32_e32 v228, v228, v228
	v_max_f32_e32 v229, v229, v229
	v_max_f32_e32 v230, v230, v230
	v_max_f32_e32 v231, v231, v231
	v_max_f32_e32 v232, v232, v232
	v_max_f32_e32 v233, v233, v233
	v_max_f32_e32 v234, v234, v234
	v_max_f32_e32 v235, v235, v235
	v_max_f32_e32 v236, v236, v236
	v_max_f32_e32 v237, v237, v237
	v_max_f32_e32 v238, v238, v238
	v_max_f32_e32 v239, v239, v239
	v_max_f32_e32 v240, v240, v240
	v_max_f32_e32 v241, v241, v241
	v_med3_f32 v226, v226, s44, v246
	v_med3_f32 v227, v227, s44, v246
	v_med3_f32 v228, v228, s44, v246
	v_med3_f32 v229, v229, s44, v246
	v_med3_f32 v230, v230, s44, v246
	v_med3_f32 v231, v231, s44, v246
	v_med3_f32 v232, v232, s44, v246
	v_med3_f32 v233, v233, s44, v246
	v_med3_f32 v234, v234, s44, v246
	v_med3_f32 v235, v235, s44, v246
	v_med3_f32 v236, v236, s44, v246
	v_med3_f32 v237, v237, s44, v246
	v_med3_f32 v238, v238, s44, v246
	v_med3_f32 v239, v239, s44, v246
	v_med3_f32 v240, v240, s44, v246
	v_med3_f32 v241, v241, s44, v246
	v_mov_b32_e32 v242, 0
	v_mov_b32_e32 v243, 0
	v_mov_b32_e32 v244, 0
	v_mov_b32_e32 v245, 0
	v_cvt_pk_fp8_f32 v242, v226, v227
	v_cvt_pk_fp8_f32 v243, v230, v231
	v_cvt_pk_fp8_f32 v244, v234, v235
	v_cvt_pk_fp8_f32 v245, v238, v239
	v_cvt_pk_fp8_f32 v242, v228, v229 op_sel:[0,0,1]
	v_cvt_pk_fp8_f32 v243, v232, v233 op_sel:[0,0,1]
	v_cvt_pk_fp8_f32 v244, v236, v237 op_sel:[0,0,1]
	v_cvt_pk_fp8_f32 v245, v240, v241 op_sel:[0,0,1]
	s_nop 0
	global_store_dwordx4 v215, v[242:245], s[6:7]
	ds_read_b32 v226, v213
	ds_read_b32 v227, v213 offset:512
	ds_read_b32 v228, v213 offset:1024
	ds_read_b32 v229, v213 offset:1536
	ds_read_b32 v230, v213 offset:2048
	ds_read_b32 v231, v213 offset:2560
	ds_read_b32 v232, v213 offset:3072
	ds_read_b32 v233, v213 offset:3584
	ds_read_b32 v234, v213 offset:4096
	ds_read_b32 v235, v213 offset:4608
	ds_read_b32 v236, v213 offset:5120
	ds_read_b32 v237, v213 offset:5632
	ds_read_b32 v238, v213 offset:6144
	ds_read_b32 v239, v213 offset:6656
	ds_read_b32 v240, v213 offset:7168
	ds_read_b32 v241, v213 offset:7680
	s_waitcnt lgkmcnt(0)
; #define GAS __attribute__((address_space(1)))
; #define LAS __attribute__((address_space(3)))
; #define LDS_WAIT() asm volatile("s_waitcnt lgkmcnt(0)" ::: "memory")
;     const int pr = item >> 1, kb = 2 * (pr / nblk) + (item & 1), nb = pr % nblk, k0 = 64 * kb, n0 = 32 * nb;
;     const int nr = n0 + (lane & 31); const int sc = MAP == 1 ? src_col_in(nr) : nr;
;     float v[32];
; #pragma unroll
;     for (int i = 0; i < 32; ++i) v[i] = sc >= 0 ? W[(size_t)(k0 + 2 * i + (lane >> 5)) * Nsrc + sc] : 0.f;
; #pragma unroll
;     for (int i = 0; i < 32; ++i) { const int k = k0 + 2 * i + (lane >> 5); float x = v[i] * wscale; if (KS) x *= (k < ksplit ? ksA[k] : ksB[k - ksplit]); scr[(2 * i + (lane >> 5)) * 33 + (lane & 31)] = x; }
;     LDS_WAIT(); asm volatile("" ::: "memory");
;     const int c = lane & 7;
; #pragma unroll
;     for (int j = 0; j < 4; ++j) { const int n = (lane >> 3) + 8 * j; const LAS float* s = scr + (8 * c) * 33 + n;
;         const unsigned long long o = (unsigned long long)pg8::pk4_fp8(s[0 * 33], s[1 * 33], s[2 * 33], s[3 * 33]) | ((unsigned long long)pg8::pk4_fp8(s[4 * 33], s[5 * 33], s[6 * 33], s[7 * 33]) << 32);
;         *(GAS unsigned long long*)(WT + (size_t)(n0 + n) * K + k0 + 8 * c) = o; }
;     LDS_WAIT(); asm volatile("" ::: "memory");
; }
	v_max_f32_e32 v226, v226, v226
	v_max_f32_e32 v227, v227, v227
	v_max_f32_e32 v228, v228, v228
	v_max_f32_e32 v229, v229, v229
	v_max_f32_e32 v230, v230, v230
	v_max_f32_e32 v231, v231, v231
	v_max_f32_e32 v232, v232, v232
	v_max_f32_e32 v233, v233, v233
	v_max_f32_e32 v234, v234, v234
	v_max_f32_e32 v235, v235, v235
	v_max_f32_e32 v236, v236, v236
	v_max_f32_e32 v237, v237, v237
	v_max_f32_e32 v238, v238, v238
	v_max_f32_e32 v239, v239, v239
	v_max_f32_e32 v240, v240, v240
	v_max_f32_e32 v241, v241, v241
	v_med3_f32 v226, v226, s44, v246
	v_med3_f32 v227, v227, s44, v246
	v_med3_f32 v228, v228, s44, v246
	v_med3_f32 v229, v229, s44, v246
	v_med3_f32 v230, v230, s44, v246
	v_med3_f32 v231, v231, s44, v246
	v_med3_f32 v232, v232, s44, v246
	v_med3_f32 v233, v233, s44, v246
	v_med3_f32 v234, v234, s44, v246
	v_med3_f32 v235, v235, s44, v246
	v_med3_f32 v236, v236, s44, v246
	v_med3_f32 v237, v237, s44, v246
	v_med3_f32 v238, v238, s44, v246
	v_med3_f32 v239, v239, s44, v246
	v_med3_f32 v240, v240, s44, v246
	v_med3_f32 v241, v241, s44, v246
	v_mov_b32_e32 v242, 0
	v_mov_b32_e32 v243, 0
	v_mov_b32_e32 v244, 0
	v_mov_b32_e32 v245, 0
	v_cvt_pk_fp8_f32 v242, v226, v227
	v_cvt_pk_fp8_f32 v243, v230, v231
	v_cvt_pk_fp8_f32 v244, v234, v235
	v_cvt_pk_fp8_f32 v245, v238, v239
	v_cvt_pk_fp8_f32 v242, v228, v229 op_sel:[0,0,1]
	v_cvt_pk_fp8_f32 v243, v232, v233 op_sel:[0,0,1]
	v_cvt_pk_fp8_f32 v244, v236, v237 op_sel:[0,0,1]
	v_cvt_pk_fp8_f32 v245, v240, v241 op_sel:[0,0,1]
	s_nop 0
	global_store_dwordx4 v216, v[242:245], s[6:7]
	s_add_u32 s6, s6, 0x400000
	s_addc_u32 s7, s7, 0
	s_waitcnt vmcnt(12)
	v_mul_f32_e32 v176, v218, v176
	v_mul_f32_e32 v177, v218, v177
	v_mul_f32_e32 v178, v218, v178
	v_mul_f32_e32 v179, v218, v179
	ds_write_b128 v210, v[176:179]
	v_mul_f32_e32 v180, v219, v180
	v_mul_f32_e32 v181, v219, v181
	v_mul_f32_e32 v182, v219, v182
	v_mul_f32_e32 v183, v219, v183
	ds_write_b128 v210, v[180:183] offset:1024
	v_mul_f32_e32 v184, v220, v184
	v_mul_f32_e32 v185, v220, v185
	v_mul_f32_e32 v186, v220, v186
	v_mul_f32_e32 v187, v220, v187
	ds_write_b128 v210, v[184:187] offset:2048
	v_mul_f32_e32 v188, v221, v188
	v_mul_f32_e32 v189, v221, v189
	v_mul_f32_e32 v190, v221, v190
	v_mul_f32_e32 v191, v221, v191
	ds_write_b128 v210, v[188:191] offset:3072
	v_mul_f32_e32 v192, v222, v192
	v_mul_f32_e32 v193, v222, v193
	v_mul_f32_e32 v194, v222, v194
	v_mul_f32_e32 v195, v222, v195
	ds_write_b128 v210, v[192:195] offset:4096
	v_mul_f32_e32 v196, v223, v196
	v_mul_f32_e32 v197, v223, v197
	v_mul_f32_e32 v198, v223, v198
	v_mul_f32_e32 v199, v223, v199
	ds_write_b128 v210, v[196:199] offset:5120
	v_mul_f32_e32 v200, v224, v200
	v_mul_f32_e32 v201, v224, v201
	v_mul_f32_e32 v202, v224, v202
	v_mul_f32_e32 v203, v224, v203
	ds_write_b128 v210, v[200:203] offset:6144
	v_mul_f32_e32 v204, v225, v204
	v_mul_f32_e32 v205, v225, v205
	v_mul_f32_e32 v206, v225, v206
	v_mul_f32_e32 v207, v225, v207
	ds_write_b128 v210, v[204:207] offset:7168
	s_waitcnt lgkmcnt(0)
	s_barrier
	s_mov_b64 s[8:9], s[4:5]
	global_load_dwordx4 v[176:179], v208, s[8:9]
	s_add_u32 s8, s8, 0x20000
	s_addc_u32 s9, s9, 0
	global_load_dwordx4 v[180:183], v208, s[8:9]
	s_add_u32 s8, s8, 0x20000
	s_addc_u32 s9, s9, 0
	global_load_dwordx4 v[184:187], v208, s[8:9]
	s_add_u32 s8, s8, 0x20000
	s_addc_u32 s9, s9, 0
	global_load_dwordx4 v[188:191], v208, s[8:9]
	s_add_u32 s8, s8, 0x20000
	s_addc_u32 s9, s9, 0
	global_load_dwordx4 v[192:195], v208, s[8:9]
	s_add_u32 s8, s8, 0x20000
	s_addc_u32 s9, s9, 0
	global_load_dwordx4 v[196:199], v208, s[8:9]
	s_add_u32 s8, s8, 0x20000
	s_addc_u32 s9, s9, 0
	global_load_dwordx4 v[200:203], v208, s[8:9]
	s_add_u32 s8, s8, 0x20000
	s_addc_u32 s9, s9, 0
	global_load_dwordx4 v[204:207], v208, s[8:9]
	s_add_u32 s4, s4, 0x1000
	s_addc_u32 s5, s5, 0
	ds_read_b32 v226, v212
	ds_read_b32 v227, v212 offset:512
	ds_read_b32 v228, v212 offset:1024
	ds_read_b32 v229, v212 offset:1536
	ds_read_b32 v230, v212 offset:2048
	ds_read_b32 v231, v212 offset:2560
	ds_read_b32 v232, v212 offset:3072
	ds_read_b32 v233, v212 offset:3584
	ds_read_b32 v234, v212 offset:4096
	ds_read_b32 v235, v212 offset:4608
	ds_read_b32 v236, v212 offset:5120
	ds_read_b32 v237, v212 offset:5632
	ds_read_b32 v238, v212 offset:6144
	ds_read_b32 v239, v212 offset:6656
	ds_read_b32 v240, v212 offset:7168
	ds_read_b32 v241, v212 offset:7680
	s_waitcnt lgkmcnt(0)
	v_max_f32_e32 v226, v226, v226
	v_max_f32_e32 v227, v227, v227
	v_max_f32_e32 v228, v228, v228
	v_max_f32_e32 v229, v229, v229
	v_max_f32_e32 v230, v230, v230
	v_max_f32_e32 v231, v231, v231
	v_max_f32_e32 v232, v232, v232
	v_max_f32_e32 v233, v233, v233
	v_max_f32_e32 v234, v234, v234
	v_max_f32_e32 v235, v235, v235
	v_max_f32_e32 v236, v236, v236
	v_max_f32_e32 v237, v237, v237
	v_max_f32_e32 v238, v238, v238
	v_max_f32_e32 v239, v239, v239
	v_max_f32_e32 v240, v240, v240
	v_max_f32_e32 v241, v241, v241
	v_med3_f32 v226, v226, s44, v246
	v_med3_f32 v227, v227, s44, v246
	v_med3_f32 v228, v228, s44, v246
	v_med3_f32 v229, v229, s44, v246
	v_med3_f32 v230, v230, s44, v246
	v_med3_f32 v231, v231, s44, v246
	v_med3_f32 v232, v232, s44, v246
	v_med3_f32 v233, v233, s44, v246
	v_med3_f32 v234, v234, s44, v246
	v_med3_f32 v235, v235, s44, v246
	v_med3_f32 v236, v236, s44, v246
	v_med3_f32 v237, v237, s44, v246
	v_med3_f32 v238, v238, s44, v246
	v_med3_f32 v239, v239, s44, v246
	v_med3_f32 v240, v240, s44, v246
	v_med3_f32 v241, v241, s44, v246
	v_mov_b32_e32 v242, 0
	v_mov_b32_e32 v243, 0
	v_mov_b32_e32 v244, 0
	v_mov_b32_e32 v245, 0
	v_cvt_pk_fp8_f32 v242, v226, v227
	v_cvt_pk_fp8_f32 v243, v230, v231
	v_cvt_pk_fp8_f32 v244, v234, v235
	v_cvt_pk_fp8_f32 v245, v238, v239
	v_cvt_pk_fp8_f32 v242, v228, v229 op_sel:[0,0,1]
	v_cvt_pk_fp8_f32 v243, v232, v233 op_sel:[0,0,1]
	v_cvt_pk_fp8_f32 v244, v236, v237 op_sel:[0,0,1]
	v_cvt_pk_fp8_f32 v245, v240, v241 op_sel:[0,0,1]
	s_nop 0
	global_store_dwordx4 v215, v[242:245], s[6:7]
	ds_read_b32 v226, v214
	ds_read_b32 v227, v214 offset:512
	ds_read_b32 v228, v214 offset:1024
	ds_read_b32 v229, v214 offset:1536
	ds_read_b32 v230, v214 offset:2048
	ds_read_b32 v231, v214 offset:2560
	ds_read_b32 v232, v214 offset:3072
	ds_read_b32 v233, v214 offset:3584
	ds_read_b32 v234, v214 offset:4096
	ds_read_b32 v235, v214 offset:4608
	ds_read_b32 v236, v214 offset:5120
	ds_read_b32 v237, v214 offset:5632
	ds_read_b32 v238, v214 offset:6144
	ds_read_b32 v239, v214 offset:6656
	ds_read_b32 v240, v214 offset:7168
	ds_read_b32 v241, v214 offset:7680
	s_waitcnt lgkmcnt(0)
; #define GAS __attribute__((address_space(1)))
; #define LAS __attribute__((address_space(3)))
; #define LDS_WAIT() asm volatile("s_waitcnt lgkmcnt(0)" ::: "memory")
;     const int pr = item >> 1, kb = 2 * (pr / nblk) + (item & 1), nb = pr % nblk, k0 = 64 * kb, n0 = 32 * nb;
;     const int nr = n0 + (lane & 31); const int sc = MAP == 1 ? src_col_in(nr) : nr;
;     float v[32];
; #pragma unroll
;     for (int i = 0; i < 32; ++i) v[i] = sc >= 0 ? W[(size_t)(k0 + 2 * i + (lane >> 5)) * Nsrc + sc] : 0.f;
; #pragma unroll
;     for (int i = 0; i < 32; ++i) { const int k = k0 + 2 * i + (lane >> 5); float x = v[i] * wscale; if (KS) x *= (k < ksplit ? ksA[k] : ksB[k - ksplit]); scr[(2 * i + (lane >> 5)) * 33 + (lane & 31)] = x; }
;     LDS_WAIT(); asm volatile("" ::: "memory");
;     const int c = lane & 7;
; #pragma unroll
;     for (int j = 0; j < 4; ++j) { const int n = (lane >> 3) + 8 * j; const LAS float* s = scr + (8 * c) * 33 + n;
;         const unsigned long long o = (unsigned long long)pg8::pk4_fp8(s[0 * 33], s[1 * 33], s[2 * 33], s[3 * 33]) | ((unsigned long long)pg8::pk4_fp8(s[4 * 33], s[5 * 33], s[6 * 33], s[7 * 33]) << 32);
;         *(GAS unsigned long long*)(WT + (size_t)(n0 + n) * K + k0 + 8 * c) = o; }
;     LDS_WAIT(); asm volatile("" ::: "memory");
; }
; __global__ void __launch_bounds__(NWAVES * 64, 2) hybrid_fwd(Args args) {
;     ...
;             if (r < I_UP) { p0_transpose_item_f8<true>(args.in[15] + (size_t)l * DM * FF, DM, FF, FF / 32, (unsigned char*)(ws + WS_WUP + l * SZ_WUP), WUP8_SCALE, args.in[14] + l * DM, args.in[14] + l * DM, DM, scr, r, lane); continue; } r -= I_UP;
	v_max_f32_e32 v226, v226, v226
	v_max_f32_e32 v227, v227, v227
	v_max_f32_e32 v228, v228, v228
	v_max_f32_e32 v229, v229, v229
	v_max_f32_e32 v230, v230, v230
	v_max_f32_e32 v231, v231, v231
	v_max_f32_e32 v232, v232, v232
	v_max_f32_e32 v233, v233, v233
	v_max_f32_e32 v234, v234, v234
	v_max_f32_e32 v235, v235, v235
	v_max_f32_e32 v236, v236, v236
	v_max_f32_e32 v237, v237, v237
	v_max_f32_e32 v238, v238, v238
	v_max_f32_e32 v239, v239, v239
	v_max_f32_e32 v240, v240, v240
	v_max_f32_e32 v241, v241, v241
	v_med3_f32 v226, v226, s44, v246
	v_med3_f32 v227, v227, s44, v246
	v_med3_f32 v228, v228, s44, v246
	v_med3_f32 v229, v229, s44, v246
	v_med3_f32 v230, v230, s44, v246
	v_med3_f32 v231, v231, s44, v246
	v_med3_f32 v232, v232, s44, v246
	v_med3_f32 v233, v233, s44, v246
	v_med3_f32 v234, v234, s44, v246
	v_med3_f32 v235, v235, s44, v246
	v_med3_f32 v236, v236, s44, v246
	v_med3_f32 v237, v237, s44, v246
	v_med3_f32 v238, v238, s44, v246
	v_med3_f32 v239, v239, s44, v246
	v_med3_f32 v240, v240, s44, v246
	v_med3_f32 v241, v241, s44, v246
	v_mov_b32_e32 v242, 0
	v_mov_b32_e32 v243, 0
	v_mov_b32_e32 v244, 0
	v_mov_b32_e32 v245, 0
	v_cvt_pk_fp8_f32 v242, v226, v227
	v_cvt_pk_fp8_f32 v243, v230, v231
	v_cvt_pk_fp8_f32 v244, v234, v235
	v_cvt_pk_fp8_f32 v245, v238, v239
	v_cvt_pk_fp8_f32 v242, v228, v229 op_sel:[0,0,1]
	v_cvt_pk_fp8_f32 v243, v232, v233 op_sel:[0,0,1]
	v_cvt_pk_fp8_f32 v244, v236, v237 op_sel:[0,0,1]
	v_cvt_pk_fp8_f32 v245, v240, v241 op_sel:[0,0,1]
	s_nop 0
	global_store_dwordx4 v216, v[242:245], s[6:7]
	s_add_u32 s6, s6, 0x400000
	s_addc_u32 s7, s7, 0
	s_sub_i32 s12, s12, 1
	s_cmp_lg_u32 s12, 0
	s_cbranch_scc1 .Lco_wup_loop
	s_waitcnt vmcnt(12)
	v_mul_f32_e32 v144, v218, v144
	v_mul_f32_e32 v145, v218, v145
	v_mul_f32_e32 v146, v218, v146
	v_mul_f32_e32 v147, v218, v147
	ds_write_b128 v209, v[144:147]
	v_mul_f32_e32 v148, v219, v148
	v_mul_f32_e32 v149, v219, v149
	v_mul_f32_e32 v150, v219, v150
	v_mul_f32_e32 v151, v219, v151
	ds_write_b128 v209, v[148:151] offset:1024
	v_mul_f32_e32 v152, v220, v152
	v_mul_f32_e32 v153, v220, v153
	v_mul_f32_e32 v154, v220, v154
	v_mul_f32_e32 v155, v220, v155
	ds_write_b128 v209, v[152:155] offset:2048
	v_mul_f32_e32 v156, v221, v156
	v_mul_f32_e32 v157, v221, v157
	v_mul_f32_e32 v158, v221, v158
	v_mul_f32_e32 v159, v221, v159
	ds_write_b128 v209, v[156:159] offset:3072
	v_mul_f32_e32 v160, v222, v160
	v_mul_f32_e32 v161, v222, v161
	v_mul_f32_e32 v162, v222, v162
	v_mul_f32_e32 v163, v222, v163
	ds_write_b128 v209, v[160:163] offset:4096
	v_mul_f32_e32 v164, v223, v164
	v_mul_f32_e32 v165, v223, v165
	v_mul_f32_e32 v166, v223, v166
	v_mul_f32_e32 v167, v223, v167
	ds_write_b128 v209, v[164:167] offset:5120
	v_mul_f32_e32 v168, v224, v168
	v_mul_f32_e32 v169, v224, v169
	v_mul_f32_e32 v170, v224, v170
	v_mul_f32_e32 v171, v224, v171
	ds_write_b128 v209, v[168:171] offset:6144
	v_mul_f32_e32 v172, v225, v172
	v_mul_f32_e32 v173, v225, v173
	v_mul_f32_e32 v174, v225, v174
	v_mul_f32_e32 v175, v225, v175
	ds_write_b128 v209, v[172:175] offset:7168
	s_waitcnt lgkmcnt(0)
	s_barrier
	ds_read_b32 v226, v211
	ds_read_b32 v227, v211 offset:512
	ds_read_b32 v228, v211 offset:1024
	ds_read_b32 v229, v211 offset:1536
	ds_read_b32 v230, v211 offset:2048
	ds_read_b32 v231, v211 offset:2560
	ds_read_b32 v232, v211 offset:3072
	ds_read_b32 v233, v211 offset:3584
	ds_read_b32 v234, v211 offset:4096
	ds_read_b32 v235, v211 offset:4608
	ds_read_b32 v236, v211 offset:5120
	ds_read_b32 v237, v211 offset:5632
	ds_read_b32 v238, v211 offset:6144
	ds_read_b32 v239, v211 offset:6656
	ds_read_b32 v240, v211 offset:7168
	ds_read_b32 v241, v211 offset:7680
	s_waitcnt lgkmcnt(0)
	v_max_f32_e32 v226, v226, v226
	v_max_f32_e32 v227, v227, v227
	v_max_f32_e32 v228, v228, v228
	v_max_f32_e32 v229, v229, v229
	v_max_f32_e32 v230, v230, v230
	v_max_f32_e32 v231, v231, v231
	v_max_f32_e32 v232, v232, v232
	v_max_f32_e32 v233, v233, v233
	v_max_f32_e32 v234, v234, v234
	v_max_f32_e32 v235, v235, v235
	v_max_f32_e32 v236, v236, v236
	v_max_f32_e32 v237, v237, v237
	v_max_f32_e32 v238, v238, v238
	v_max_f32_e32 v239, v239, v239
	v_max_f32_e32 v240, v240, v240
	v_max_f32_e32 v241, v241, v241
	v_med3_f32 v226, v226, s44, v246
	v_med3_f32 v227, v227, s44, v246
	v_med3_f32 v228, v228, s44, v246
	v_med3_f32 v229, v229, s44, v246
	v_med3_f32 v230, v230, s44, v246
	v_med3_f32 v231, v231, s44, v246
	v_med3_f32 v232, v232, s44, v246
	v_med3_f32 v233, v233, s44, v246
	v_med3_f32 v234, v234, s44, v246
	v_med3_f32 v235, v235, s44, v246
	v_med3_f32 v236, v236, s44, v246
	v_med3_f32 v237, v237, s44, v246
	v_med3_f32 v238, v238, s44, v246
	v_med3_f32 v239, v239, s44, v246
	v_med3_f32 v240, v240, s44, v246
	v_med3_f32 v241, v241, s44, v246
	v_mov_b32_e32 v242, 0
	v_mov_b32_e32 v243, 0
	v_mov_b32_e32 v244, 0
	v_mov_b32_e32 v245, 0
	v_cvt_pk_fp8_f32 v242, v226, v227
	v_cvt_pk_fp8_f32 v243, v230, v231
	v_cvt_pk_fp8_f32 v244, v234, v235
	v_cvt_pk_fp8_f32 v245, v238, v239
	v_cvt_pk_fp8_f32 v242, v228, v229 op_sel:[0,0,1]
	v_cvt_pk_fp8_f32 v243, v232, v233 op_sel:[0,0,1]
	v_cvt_pk_fp8_f32 v244, v236, v237 op_sel:[0,0,1]
	v_cvt_pk_fp8_f32 v245, v240, v241 op_sel:[0,0,1]
	s_nop 0
	global_store_dwordx4 v215, v[242:245], s[6:7]
	ds_read_b32 v226, v213
	ds_read_b32 v227, v213 offset:512
	ds_read_b32 v228, v213 offset:1024
	ds_read_b32 v229, v213 offset:1536
	ds_read_b32 v230, v213 offset:2048
	ds_read_b32 v231, v213 offset:2560
	ds_read_b32 v232, v213 offset:3072
	ds_read_b32 v233, v213 offset:3584
	ds_read_b32 v234, v213 offset:4096
	ds_read_b32 v235, v213 offset:4608
	ds_read_b32 v236, v213 offset:5120
	ds_read_b32 v237, v213 offset:5632
	ds_read_b32 v238, v213 offset:6144
	ds_read_b32 v239, v213 offset:6656
	ds_read_b32 v240, v213 offset:7168
	ds_read_b32 v241, v213 offset:7680
	s_waitcnt lgkmcnt(0)
; #define GAS __attribute__((address_space(1)))
; #define LAS __attribute__((address_space(3)))
; #define LDS_WAIT() asm volatile("s_waitcnt lgkmcnt(0)" ::: "memory")
;     const int pr = item >> 1, kb = 2 * (pr / nblk) + (item & 1), nb = pr % nblk, k0 = 64 * kb, n0 = 32 * nb;
;     const int nr = n0 + (lane & 31); const int sc = MAP == 1 ? src_col_in(nr) : nr;
;     float v[32];
; #pragma unroll
;     for (int i = 0; i < 32; ++i) v[i] = sc >= 0 ? W[(size_t)(k0 + 2 * i + (lane >> 5)) * Nsrc + sc] : 0.f;
; #pragma unroll
;     for (int i = 0; i < 32; ++i) { const int k = k0 + 2 * i + (lane >> 5); float x = v[i] * wscale; if (KS) x *= (k < ksplit ? ksA[k] : ksB[k - ksplit]); scr[(2 * i + (lane >> 5)) * 33 + (lane & 31)] = x; }
;     LDS_WAIT(); asm volatile("" ::: "memory");
;     const int c = lane & 7;
; #pragma unroll
;     for (int j = 0; j < 4; ++j) { const int n = (lane >> 3) + 8 * j; const LAS float* s = scr + (8 * c) * 33 + n;
;         const unsigned long long o = (unsigned long long)pg8::pk4_fp8(s[0 * 33], s[1 * 33], s[2 * 33], s[3 * 33]) | ((unsigned long long)pg8::pk4_fp8(s[4 * 33], s[5 * 33], s[6 * 33], s[7 * 33]) << 32);
;         *(GAS unsigned long long*)(WT + (size_t)(n0 + n) * K + k0 + 8 * c) = o; }
;     LDS_WAIT(); asm volatile("" ::: "memory");
; }
; __global__ void __launch_bounds__(NWAVES * 64, 2) hybrid_fwd(Args args) {
;     ...
;             if (r < I_UP) { p0_transpose_item_f8<true>(args.in[15] + (size_t)l * DM * FF, DM, FF, FF / 32, (unsigned char*)(ws + WS_WUP + l * SZ_WUP), WUP8_SCALE, args.in[14] + l * DM, args.in[14] + l * DM, DM, scr, r, lane); continue; } r -= I_UP;
	v_max_f32_e32 v226, v226, v226
	v_max_f32_e32 v227, v227, v227
	v_max_f32_e32 v228, v228, v228
	v_max_f32_e32 v229, v229, v229
	v_max_f32_e32 v230, v230, v230
	v_max_f32_e32 v231, v231, v231
	v_max_f32_e32 v232, v232, v232
	v_max_f32_e32 v233, v233, v233
	v_max_f32_e32 v234, v234, v234
	v_max_f32_e32 v235, v235, v235
	v_max_f32_e32 v236, v236, v236
	v_max_f32_e32 v237, v237, v237
	v_max_f32_e32 v238, v238, v238
	v_max_f32_e32 v239, v239, v239
	v_max_f32_e32 v240, v240, v240
	v_max_f32_e32 v241, v241, v241
	v_med3_f32 v226, v226, s44, v246
	v_med3_f32 v227, v227, s44, v246
	v_med3_f32 v228, v228, s44, v246
	v_med3_f32 v229, v229, s44, v246
	v_med3_f32 v230, v230, s44, v246
	v_med3_f32 v231, v231, s44, v246
	v_med3_f32 v232, v232, s44, v246
	v_med3_f32 v233, v233, s44, v246
	v_med3_f32 v234, v234, s44, v246
	v_med3_f32 v235, v235, s44, v246
	v_med3_f32 v236, v236, s44, v246
	v_med3_f32 v237, v237, s44, v246
	v_med3_f32 v238, v238, s44, v246
	v_med3_f32 v239, v239, s44, v246
	v_med3_f32 v240, v240, s44, v246
	v_med3_f32 v241, v241, s44, v246
	v_mov_b32_e32 v242, 0
	v_mov_b32_e32 v243, 0
	v_mov_b32_e32 v244, 0
	v_mov_b32_e32 v245, 0
	v_cvt_pk_fp8_f32 v242, v226, v227
	v_cvt_pk_fp8_f32 v243, v230, v231
	v_cvt_pk_fp8_f32 v244, v234, v235
	v_cvt_pk_fp8_f32 v245, v238, v239
	v_cvt_pk_fp8_f32 v242, v228, v229 op_sel:[0,0,1]
	v_cvt_pk_fp8_f32 v243, v232, v233 op_sel:[0,0,1]
	v_cvt_pk_fp8_f32 v244, v236, v237 op_sel:[0,0,1]
	v_cvt_pk_fp8_f32 v245, v240, v241 op_sel:[0,0,1]
	s_nop 0
	global_store_dwordx4 v216, v[242:245], s[6:7]
	s_add_u32 s6, s6, 0x400000
	s_addc_u32 s7, s7, 0
	s_waitcnt vmcnt(4)
	v_mul_f32_e32 v176, v218, v176
	v_mul_f32_e32 v177, v218, v177
	v_mul_f32_e32 v178, v218, v178
	v_mul_f32_e32 v179, v218, v179
	ds_write_b128 v210, v[176:179]
	v_mul_f32_e32 v180, v219, v180
	v_mul_f32_e32 v181, v219, v181
	v_mul_f32_e32 v182, v219, v182
	v_mul_f32_e32 v183, v219, v183
	ds_write_b128 v210, v[180:183] offset:1024
	v_mul_f32_e32 v184, v220, v184
	v_mul_f32_e32 v185, v220, v185
	v_mul_f32_e32 v186, v220, v186
	v_mul_f32_e32 v187, v220, v187
	ds_write_b128 v210, v[184:187] offset:2048
	v_mul_f32_e32 v188, v221, v188
	v_mul_f32_e32 v189, v221, v189
	v_mul_f32_e32 v190, v221, v190
	v_mul_f32_e32 v191, v221, v191
	ds_write_b128 v210, v[188:191] offset:3072
	v_mul_f32_e32 v192, v222, v192
	v_mul_f32_e32 v193, v222, v193
	v_mul_f32_e32 v194, v222, v194
	v_mul_f32_e32 v195, v222, v195
	ds_write_b128 v210, v[192:195] offset:4096
	v_mul_f32_e32 v196, v223, v196
	v_mul_f32_e32 v197, v223, v197
	v_mul_f32_e32 v198, v223, v198
	v_mul_f32_e32 v199, v223, v199
	ds_write_b128 v210, v[196:199] offset:5120
	v_mul_f32_e32 v200, v224, v200
	v_mul_f32_e32 v201, v224, v201
	v_mul_f32_e32 v202, v224, v202
	v_mul_f32_e32 v203, v224, v203
	ds_write_b128 v210, v[200:203] offset:6144
	v_mul_f32_e32 v204, v225, v204
	v_mul_f32_e32 v205, v225, v205
	v_mul_f32_e32 v206, v225, v206
	v_mul_f32_e32 v207, v225, v207
	ds_write_b128 v210, v[204:207] offset:7168
	s_waitcnt lgkmcnt(0)
	s_barrier
	ds_read_b32 v226, v212
	ds_read_b32 v227, v212 offset:512
	ds_read_b32 v228, v212 offset:1024
	ds_read_b32 v229, v212 offset:1536
	ds_read_b32 v230, v212 offset:2048
	ds_read_b32 v231, v212 offset:2560
	ds_read_b32 v232, v212 offset:3072
	ds_read_b32 v233, v212 offset:3584
	ds_read_b32 v234, v212 offset:4096
	ds_read_b32 v235, v212 offset:4608
	ds_read_b32 v236, v212 offset:5120
	ds_read_b32 v237, v212 offset:5632
	ds_read_b32 v238, v212 offset:6144
	ds_read_b32 v239, v212 offset:6656
	ds_read_b32 v240, v212 offset:7168
	ds_read_b32 v241, v212 offset:7680
	s_waitcnt lgkmcnt(0)
	v_max_f32_e32 v226, v226, v226
	v_max_f32_e32 v227, v227, v227
	v_max_f32_e32 v228, v228, v228
	v_max_f32_e32 v229, v229, v229
	v_max_f32_e32 v230, v230, v230
	v_max_f32_e32 v231, v231, v231
	v_max_f32_e32 v232, v232, v232
	v_max_f32_e32 v233, v233, v233
	v_max_f32_e32 v234, v234, v234
	v_max_f32_e32 v235, v235, v235
	v_max_f32_e32 v236, v236, v236
	v_max_f32_e32 v237, v237, v237
	v_max_f32_e32 v238, v238, v238
	v_max_f32_e32 v239, v239, v239
	v_max_f32_e32 v240, v240, v240
	v_max_f32_e32 v241, v241, v241
	v_med3_f32 v226, v226, s44, v246
	v_med3_f32 v227, v227, s44, v246
	v_med3_f32 v228, v228, s44, v246
	v_med3_f32 v229, v229, s44, v246
	v_med3_f32 v230, v230, s44, v246
	v_med3_f32 v231, v231, s44, v246
	v_med3_f32 v232, v232, s44, v246
	v_med3_f32 v233, v233, s44, v246
	v_med3_f32 v234, v234, s44, v246
	v_med3_f32 v235, v235, s44, v246
	v_med3_f32 v236, v236, s44, v246
	v_med3_f32 v237, v237, s44, v246
	v_med3_f32 v238, v238, s44, v246
	v_med3_f32 v239, v239, s44, v246
	v_med3_f32 v240, v240, s44, v246
	v_med3_f32 v241, v241, s44, v246
	v_mov_b32_e32 v242, 0
	v_mov_b32_e32 v243, 0
	v_mov_b32_e32 v244, 0
	v_mov_b32_e32 v245, 0
	v_cvt_pk_fp8_f32 v242, v226, v227
	v_cvt_pk_fp8_f32 v243, v230, v231
	v_cvt_pk_fp8_f32 v244, v234, v235
	v_cvt_pk_fp8_f32 v245, v238, v239
	v_cvt_pk_fp8_f32 v242, v228, v229 op_sel:[0,0,1]
	v_cvt_pk_fp8_f32 v243, v232, v233 op_sel:[0,0,1]
	v_cvt_pk_fp8_f32 v244, v236, v237 op_sel:[0,0,1]
	v_cvt_pk_fp8_f32 v245, v240, v241 op_sel:[0,0,1]
	s_nop 0
	global_store_dwordx4 v215, v[242:245], s[6:7]
	ds_read_b32 v226, v214
	ds_read_b32 v227, v214 offset:512
	ds_read_b32 v228, v214 offset:1024
	ds_read_b32 v229, v214 offset:1536
	ds_read_b32 v230, v214 offset:2048
	ds_read_b32 v231, v214 offset:2560
	ds_read_b32 v232, v214 offset:3072
	ds_read_b32 v233, v214 offset:3584
	ds_read_b32 v234, v214 offset:4096
	ds_read_b32 v235, v214 offset:4608
	ds_read_b32 v236, v214 offset:5120
	ds_read_b32 v237, v214 offset:5632
	ds_read_b32 v238, v214 offset:6144
	ds_read_b32 v239, v214 offset:6656
	ds_read_b32 v240, v214 offset:7168
	ds_read_b32 v241, v214 offset:7680
	s_waitcnt lgkmcnt(0)
; #define GAS __attribute__((address_space(1)))
; #define LAS __attribute__((address_space(3)))
; #define LDS_WAIT() asm volatile("s_waitcnt lgkmcnt(0)" ::: "memory")
;     const int pr = item >> 1, kb = 2 * (pr / nblk) + (item & 1), nb = pr % nblk, k0 = 64 * kb, n0 = 32 * nb;
;     const int nr = n0 + (lane & 31); const int sc = MAP == 1 ? src_col_in(nr) : nr;
;     float v[32];
; #pragma unroll
;     for (int i = 0; i < 32; ++i) v[i] = sc >= 0 ? W[(size_t)(k0 + 2 * i + (lane >> 5)) * Nsrc + sc] : 0.f;
; #pragma unroll
;     for (int i = 0; i < 32; ++i) { const int k = k0 + 2 * i + (lane >> 5); float x = v[i] * wscale; if (KS) x *= (k < ksplit ? ksA[k] : ksB[k - ksplit]); scr[(2 * i + (lane >> 5)) * 33 + (lane & 31)] = x; }
;     LDS_WAIT(); asm volatile("" ::: "memory");
;     const int c = lane & 7;
; #pragma unroll
;     for (int j = 0; j < 4; ++j) { const int n = (lane >> 3) + 8 * j; const LAS float* s = scr + (8 * c) * 33 + n;
;         const unsigned long long o = (unsigned long long)pg8::pk4_fp8(s[0 * 33], s[1 * 33], s[2 * 33], s[3 * 33]) | ((unsigned long long)pg8::pk4_fp8(s[4 * 33], s[5 * 33], s[6 * 33], s[7 * 33]) << 32);
;         *(GAS unsigned long long*)(WT + (size_t)(n0 + n) * K + k0 + 8 * c) = o; }
;     LDS_WAIT(); asm volatile("" ::: "memory");
; }
; __global__ void __launch_bounds__(NWAVES * 64, 2) hybrid_fwd(Args args) {
;     ...
;             p0_transpose_item_f8<false>(args.in[16] + (size_t)l * FF * DM, FF, DM, DM / 32, (unsigned char*)(ws + WS_WDN + l * SZ_WDN), 128.f, args.in[16], args.in[16], 0, scr, r, lane);
	v_max_f32_e32 v226, v226, v226
	v_max_f32_e32 v227, v227, v227
	v_max_f32_e32 v228, v228, v228
	v_max_f32_e32 v229, v229, v229
	v_max_f32_e32 v230, v230, v230
	v_max_f32_e32 v231, v231, v231
	v_max_f32_e32 v232, v232, v232
	v_max_f32_e32 v233, v233, v233
	v_max_f32_e32 v234, v234, v234
	v_max_f32_e32 v235, v235, v235
	v_max_f32_e32 v236, v236, v236
	v_max_f32_e32 v237, v237, v237
	v_max_f32_e32 v238, v238, v238
	v_max_f32_e32 v239, v239, v239
	v_max_f32_e32 v240, v240, v240
	v_max_f32_e32 v241, v241, v241
	v_med3_f32 v226, v226, s44, v246
	v_med3_f32 v227, v227, s44, v246
	v_med3_f32 v228, v228, s44, v246
	v_med3_f32 v229, v229, s44, v246
	v_med3_f32 v230, v230, s44, v246
	v_med3_f32 v231, v231, s44, v246
	v_med3_f32 v232, v232, s44, v246
	v_med3_f32 v233, v233, s44, v246
	v_med3_f32 v234, v234, s44, v246
	v_med3_f32 v235, v235, s44, v246
	v_med3_f32 v236, v236, s44, v246
	v_med3_f32 v237, v237, s44, v246
	v_med3_f32 v238, v238, s44, v246
	v_med3_f32 v239, v239, s44, v246
	v_med3_f32 v240, v240, s44, v246
	v_med3_f32 v241, v241, s44, v246
	v_mov_b32_e32 v242, 0
	v_mov_b32_e32 v243, 0
	v_mov_b32_e32 v244, 0
	v_mov_b32_e32 v245, 0
	v_cvt_pk_fp8_f32 v242, v226, v227
	v_cvt_pk_fp8_f32 v243, v230, v231
	v_cvt_pk_fp8_f32 v244, v234, v235
	v_cvt_pk_fp8_f32 v245, v238, v239
	v_cvt_pk_fp8_f32 v242, v228, v229 op_sel:[0,0,1]
	v_cvt_pk_fp8_f32 v243, v232, v233 op_sel:[0,0,1]
	v_cvt_pk_fp8_f32 v244, v236, v237 op_sel:[0,0,1]
	v_cvt_pk_fp8_f32 v245, v240, v241 op_sel:[0,0,1]
	s_nop 0
	global_store_dwordx4 v216, v[242:245], s[6:7]
	s_add_u32 s6, s6, 0x400000
	s_addc_u32 s7, s7, 0
	s_add_u32 s16, s16, 0x10000000
	s_addc_u32 s17, s17, 0
	s_add_u32 s18, s18, 0x8000000
	s_addc_u32 s19, s19, 0
	s_add_u32 s10, s10, 0x4000
	s_addc_u32 s11, s11, 0
	s_add_i32 s13, s13, 1
	s_cmp_lg_u32 s13, 2
	s_cbranch_scc1 .Lco_wup_layer
	v_lshrrev_b32_e32 v246, 5, v249
	v_lshl_add_u32 v246, v250, 4, v246
	v_and_b32_e32 v247, 31, v249
	v_lshlrev_b32_e32 v247, 4, v247
	v_lshl_add_u32 v208, v246, 14, v247
	v_lshrrev_b32_e32 v246, 3, v249
	v_lshl_add_u32 v246, v250, 4, v246
	v_and_b32_e32 v247, 7, v249
	v_lshlrev_b32_e32 v247, 4, v247
	v_lshl_add_u32 v215, v246, 14, v247
	v_add_u32_e32 v216, 0x20000, v215
	s_lshr_b32 s22, s15, 3
	s_and_b32 s23, s15, 7
	v_readlane_b32 s16, v253, 35
	v_readlane_b32 s17, v253, 36
	v_readlane_b32 s18, v253, 41
	v_readlane_b32 s19, v253, 42
	s_lshl_b32 s20, s22, 21
	s_lshl_b32 s21, s23, 9
	s_add_u32 s20, s20, s21
	s_add_u32 s16, s16, s20
	s_addc_u32 s17, s17, 0
	s_add_u32 s18, s18, 0x1f600000
	s_addc_u32 s19, s19, 0
	s_lshl_b32 s20, s23, 21
	s_lshl_b32 s21, s22, 7
	s_add_u32 s20, s20, s21
	s_add_u32 s18, s18, s20
	s_addc_u32 s19, s19, 0
	s_mov_b32 s13, 0
.Lco_wdn_layer:
	s_mov_b64 s[4:5], s[16:17]
	s_mov_b64 s[6:7], s[18:19]
	s_mov_b32 s24, 0
	s_mov_b32 s25, 0
	s_mov_b32 s44, 0xc3e00000
	v_mov_b32_e32 v246, 0x43e00000
	s_mov_b64 s[8:9], s[4:5]
	global_load_dwordx4 v[144:147], v208, s[8:9]
	s_add_u32 s8, s8, 0x8000
	s_addc_u32 s9, s9, 0
	global_load_dwordx4 v[148:151], v208, s[8:9]
	s_add_u32 s8, s8, 0x8000
	s_addc_u32 s9, s9, 0
	global_load_dwordx4 v[152:155], v208, s[8:9]
	s_add_u32 s8, s8, 0x8000
	s_addc_u32 s9, s9, 0
	global_load_dwordx4 v[156:159], v208, s[8:9]
	s_add_u32 s8, s8, 0x8000
	s_addc_u32 s9, s9, 0
	global_load_dwordx4 v[160:163], v208, s[8:9]
	s_add_u32 s8, s8, 0x8000
	s_addc_u32 s9, s9, 0
	global_load_dwordx4 v[164:167], v208, s[8:9]
	s_add_u32 s8, s8, 0x8000
	s_addc_u32 s9, s9, 0
	global_load_dwordx4 v[168:171], v208, s[8:9]
	s_add_u32 s8, s8, 0x8000
	s_addc_u32 s9, s9, 0
	global_load_dwordx4 v[172:175], v208, s[8:9]
	s_add_i32 s24, s24, 1
	s_and_b32 s26, s24, 3
	s_cmp_eq_u32 s26, 0
	s_mov_b32 s26, 0x3ffd000
	s_cselect_b32 s26, s26, 0x1000
	s_add_u32 s4, s4, s26
	s_addc_u32 s5, s5, 0
	s_mov_b64 s[8:9], s[4:5]
	global_load_dwordx4 v[176:179], v208, s[8:9]
	s_add_u32 s8, s8, 0x8000
	s_addc_u32 s9, s9, 0
	global_load_dwordx4 v[180:183], v208, s[8:9]
	s_add_u32 s8, s8, 0x8000
	s_addc_u32 s9, s9, 0
	global_load_dwordx4 v[184:187], v208, s[8:9]
	s_add_u32 s8, s8, 0x8000
	s_addc_u32 s9, s9, 0
	global_load_dwordx4 v[188:191], v208, s[8:9]
	s_add_u32 s8, s8, 0x8000
	s_addc_u32 s9, s9, 0
	global_load_dwordx4 v[192:195], v208, s[8:9]
	s_add_u32 s8, s8, 0x8000
	s_addc_u32 s9, s9, 0
	global_load_dwordx4 v[196:199], v208, s[8:9]
	s_add_u32 s8, s8, 0x8000
	s_addc_u32 s9, s9, 0
	global_load_dwordx4 v[200:203], v208, s[8:9]
	s_add_u32 s8, s8, 0x8000
	s_addc_u32 s9, s9, 0
	global_load_dwordx4 v[204:207], v208, s[8:9]
	s_add_i32 s24, s24, 1
	s_and_b32 s26, s24, 3
	s_cmp_eq_u32 s26, 0
	s_mov_b32 s26, 0x3ffd000
	s_cselect_b32 s26, s26, 0x1000
	s_add_u32 s4, s4, s26
	s_addc_u32 s5, s5, 0
	s_waitcnt vmcnt(8)
	v_mul_f32_e32 v144, 0x43000000, v144
	v_mul_f32_e32 v145, 0x43000000, v145
	v_mul_f32_e32 v146, 0x43000000, v146
	v_mul_f32_e32 v147, 0x43000000, v147
	ds_write_b128 v209, v[144:147]
	v_mul_f32_e32 v148, 0x43000000, v148
	v_mul_f32_e32 v149, 0x43000000, v149
	v_mul_f32_e32 v150, 0x43000000, v150
	v_mul_f32_e32 v151, 0x43000000, v151
	ds_write_b128 v209, v[148:151] offset:1024
	v_mul_f32_e32 v152, 0x43000000, v152
	v_mul_f32_e32 v153, 0x43000000, v153
	v_mul_f32_e32 v154, 0x43000000, v154
	v_mul_f32_e32 v155, 0x43000000, v155
	ds_write_b128 v209, v[152:155] offset:2048
	v_mul_f32_e32 v156, 0x43000000, v156
	v_mul_f32_e32 v157, 0x43000000, v157
	v_mul_f32_e32 v158, 0x43000000, v158
	v_mul_f32_e32 v159, 0x43000000, v159
	ds_write_b128 v209, v[156:159] offset:3072
	v_mul_f32_e32 v160, 0x43000000, v160
	v_mul_f32_e32 v161, 0x43000000, v161
	v_mul_f32_e32 v162, 0x43000000, v162
	v_mul_f32_e32 v163, 0x43000000, v163
	ds_write_b128 v209, v[160:163] offset:4096
	v_mul_f32_e32 v164, 0x43000000, v164
	v_mul_f32_e32 v165, 0x43000000, v165
	v_mul_f32_e32 v166, 0x43000000, v166
	v_mul_f32_e32 v167, 0x43000000, v167
	ds_write_b128 v209, v[164:167] offset:5120
	v_mul_f32_e32 v168, 0x43000000, v168
	v_mul_f32_e32 v169, 0x43000000, v169
	v_mul_f32_e32 v170, 0x43000000, v170
	v_mul_f32_e32 v171, 0x43000000, v171
	ds_write_b128 v209, v[168:171] offset:6144
	v_mul_f32_e32 v172, 0x43000000, v172
	v_mul_f32_e32 v173, 0x43000000, v173
	v_mul_f32_e32 v174, 0x43000000, v174
	v_mul_f32_e32 v175, 0x43000000, v175
	ds_write_b128 v209, v[172:175] offset:7168
	s_waitcnt lgkmcnt(0)
	s_barrier
; #define GAS __attribute__((address_space(1)))
; #define LAS __attribute__((address_space(3)))
; #define LDS_WAIT() asm volatile("s_waitcnt lgkmcnt(0)" ::: "memory")
;     const int pr = item >> 1, kb = 2 * (pr / nblk) + (item & 1), nb = pr % nblk, k0 = 64 * kb, n0 = 32 * nb;
;     const int nr = n0 + (lane & 31); const int sc = MAP == 1 ? src_col_in(nr) : nr;
;     float v[32];
; #pragma unroll
;     for (int i = 0; i < 32; ++i) v[i] = sc >= 0 ? W[(size_t)(k0 + 2 * i + (lane >> 5)) * Nsrc + sc] : 0.f;
; #pragma unroll
;     for (int i = 0; i < 32; ++i) { const int k = k0 + 2 * i + (lane >> 5); float x = v[i] * wscale; if (KS) x *= (k < ksplit ? ksA[k] : ksB[k - ksplit]); scr[(2 * i + (lane >> 5)) * 33 + (lane & 31)] = x; }
;     LDS_WAIT(); asm volatile("" ::: "memory");
;     const int c = lane & 7;
; #pragma unroll
;     for (int j = 0; j < 4; ++j) { const int n = (lane >> 3) + 8 * j; const LAS float* s = scr + (8 * c) * 33 + n;
;         const unsigned long long o = (unsigned long long)pg8::pk4_fp8(s[0 * 33], s[1 * 33], s[2 * 33], s[3 * 33]) | ((unsigned long long)pg8::pk4_fp8(s[4 * 33], s[5 * 33], s[6 * 33], s[7 * 33]) << 32);
;         *(GAS unsigned long long*)(WT + (size_t)(n0 + n) * K + k0 + 8 * c) = o; }
;     LDS_WAIT(); asm volatile("" ::: "memory");
; }
; __global__ void __launch_bounds__(NWAVES * 64, 2) hybrid_fwd(Args args) {
;     ...
;             p0_transpose_item_f8<false>(args.in[16] + (size_t)l * FF * DM, FF, DM, DM / 32, (unsigned char*)(ws + WS_WDN + l * SZ_WDN), 128.f, args.in[16], args.in[16], 0, scr, r, lane);
	s_mov_b64 s[8:9], s[4:5]
	global_load_dwordx4 v[144:147], v208, s[8:9]
	s_add_u32 s8, s8, 0x8000
	s_addc_u32 s9, s9, 0
	global_load_dwordx4 v[148:151], v208, s[8:9]
	s_add_u32 s8, s8, 0x8000
	s_addc_u32 s9, s9, 0
	global_load_dwordx4 v[152:155], v208, s[8:9]
	s_add_u32 s8, s8, 0x8000
	s_addc_u32 s9, s9, 0
	global_load_dwordx4 v[156:159], v208, s[8:9]
	s_add_u32 s8, s8, 0x8000
	s_addc_u32 s9, s9, 0
	global_load_dwordx4 v[160:163], v208, s[8:9]
	s_add_u32 s8, s8, 0x8000
	s_addc_u32 s9, s9, 0
	global_load_dwordx4 v[164:167], v208, s[8:9]
	s_add_u32 s8, s8, 0x8000
	s_addc_u32 s9, s9, 0
	global_load_dwordx4 v[168:171], v208, s[8:9]
	s_add_u32 s8, s8, 0x8000
	s_addc_u32 s9, s9, 0
	global_load_dwordx4 v[172:175], v208, s[8:9]
	s_add_i32 s24, s24, 1
	s_and_b32 s26, s24, 3
	s_cmp_eq_u32 s26, 0
	s_mov_b32 s26, 0x3ffd000
	s_cselect_b32 s26, s26, 0x1000
	s_add_u32 s4, s4, s26
	s_addc_u32 s5, s5, 0
	ds_read_b32 v226, v211
	ds_read_b32 v227, v211 offset:512
	ds_read_b32 v228, v211 offset:1024
	ds_read_b32 v229, v211 offset:1536
	ds_read_b32 v230, v211 offset:2048
	ds_read_b32 v231, v211 offset:2560
	ds_read_b32 v232, v211 offset:3072
	ds_read_b32 v233, v211 offset:3584
	ds_read_b32 v234, v211 offset:4096
	ds_read_b32 v235, v211 offset:4608
	ds_read_b32 v236, v211 offset:5120
	ds_read_b32 v237, v211 offset:5632
	ds_read_b32 v238, v211 offset:6144
	ds_read_b32 v239, v211 offset:6656
	ds_read_b32 v240, v211 offset:7168
	ds_read_b32 v241, v211 offset:7680
	s_waitcnt lgkmcnt(0)
	v_max_f32_e32 v226, v226, v226
	v_max_f32_e32 v227, v227, v227
	v_max_f32_e32 v228, v228, v228
	v_max_f32_e32 v229, v229, v229
	v_max_f32_e32 v230, v230, v230
	v_max_f32_e32 v231, v231, v231
	v_max_f32_e32 v232, v232, v232
	v_max_f32_e32 v233, v233, v233
	v_max_f32_e32 v234, v234, v234
	v_max_f32_e32 v235, v235, v235
	v_max_f32_e32 v236, v236, v236
	v_max_f32_e32 v237, v237, v237
	v_max_f32_e32 v238, v238, v238
	v_max_f32_e32 v239, v239, v239
	v_max_f32_e32 v240, v240, v240
	v_max_f32_e32 v241, v241, v241
	v_med3_f32 v226, v226, s44, v246
	v_med3_f32 v227, v227, s44, v246
	v_med3_f32 v228, v228, s44, v246
	v_med3_f32 v229, v229, s44, v246
	v_med3_f32 v230, v230, s44, v246
	v_med3_f32 v231, v231, s44, v246
	v_med3_f32 v232, v232, s44, v246
	v_med3_f32 v233, v233, s44, v246
	v_med3_f32 v234, v234, s44, v246
	v_med3_f32 v235, v235, s44, v246
	v_med3_f32 v236, v236, s44, v246
	v_med3_f32 v237, v237, s44, v246
	v_med3_f32 v238, v238, s44, v246
	v_med3_f32 v239, v239, s44, v246
	v_med3_f32 v240, v240, s44, v246
	v_med3_f32 v241, v241, s44, v246
	v_mov_b32_e32 v242, 0
	v_mov_b32_e32 v243, 0
	v_mov_b32_e32 v244, 0
	v_mov_b32_e32 v245, 0
	v_cvt_pk_fp8_f32 v242, v226, v227
	v_cvt_pk_fp8_f32 v243, v230, v231
	v_cvt_pk_fp8_f32 v244, v234, v235
	v_cvt_pk_fp8_f32 v245, v238, v239
	v_cvt_pk_fp8_f32 v242, v228, v229 op_sel:[0,0,1]
	v_cvt_pk_fp8_f32 v243, v232, v233 op_sel:[0,0,1]
	v_cvt_pk_fp8_f32 v244, v236, v237 op_sel:[0,0,1]
	v_cvt_pk_fp8_f32 v245, v240, v241 op_sel:[0,0,1]
	s_nop 0
	global_store_dwordx4 v215, v[242:245], s[6:7]
	ds_read_b32 v226, v213
	ds_read_b32 v227, v213 offset:512
	ds_read_b32 v228, v213 offset:1024
	ds_read_b32 v229, v213 offset:1536
	ds_read_b32 v230, v213 offset:2048
	ds_read_b32 v231, v213 offset:2560
	ds_read_b32 v232, v213 offset:3072
	ds_read_b32 v233, v213 offset:3584
	ds_read_b32 v234, v213 offset:4096
	ds_read_b32 v235, v213 offset:4608
	ds_read_b32 v236, v213 offset:5120
	ds_read_b32 v237, v213 offset:5632
	ds_read_b32 v238, v213 offset:6144
	ds_read_b32 v239, v213 offset:6656
	ds_read_b32 v240, v213 offset:7168
	ds_read_b32 v241, v213 offset:7680
	s_waitcnt lgkmcnt(0)
	v_max_f32_e32 v226, v226, v226
	v_max_f32_e32 v227, v227, v227
	v_max_f32_e32 v228, v228, v228
	v_max_f32_e32 v229, v229, v229
	v_max_f32_e32 v230, v230, v230
	v_max_f32_e32 v231, v231, v231
	v_max_f32_e32 v232, v232, v232
	v_max_f32_e32 v233, v233, v233
	v_max_f32_e32 v234, v234, v234
	v_max_f32_e32 v235, v235, v235
	v_max_f32_e32 v236, v236, v236
	v_max_f32_e32 v237, v237, v237
	v_max_f32_e32 v238, v238, v238
	v_max_f32_e32 v239, v239, v239
	v_max_f32_e32 v240, v240, v240
	v_max_f32_e32 v241, v241, v241
	v_med3_f32 v226, v226, s44, v246
	v_med3_f32 v227, v227, s44, v246
	v_med3_f32 v228, v228, s44, v246
	v_med3_f32 v229, v229, s44, v246
	v_med3_f32 v230, v230, s44, v246
	v_med3_f32 v231, v231, s44, v246
	v_med3_f32 v232, v232, s44, v246
	v_med3_f32 v233, v233, s44, v246
	v_med3_f32 v234, v234, s44, v246
	v_med3_f32 v235, v235, s44, v246
	v_med3_f32 v236, v236, s44, v246
	v_med3_f32 v237, v237, s44, v246
	v_med3_f32 v238, v238, s44, v246
	v_med3_f32 v239, v239, s44, v246
	v_med3_f32 v240, v240, s44, v246
	v_med3_f32 v241, v241, s44, v246
	v_mov_b32_e32 v242, 0
	v_mov_b32_e32 v243, 0
	v_mov_b32_e32 v244, 0
	v_mov_b32_e32 v245, 0
	v_cvt_pk_fp8_f32 v242, v226, v227
	v_cvt_pk_fp8_f32 v243, v230, v231
	v_cvt_pk_fp8_f32 v244, v234, v235
	v_cvt_pk_fp8_f32 v245, v238, v239
	v_cvt_pk_fp8_f32 v242, v228, v229 op_sel:[0,0,1]
	v_cvt_pk_fp8_f32 v243, v232, v233 op_sel:[0,0,1]
	v_cvt_pk_fp8_f32 v244, v236, v237 op_sel:[0,0,1]
	v_cvt_pk_fp8_f32 v245, v240, v241 op_sel:[0,0,1]
	s_nop 0
	global_store_dwordx4 v216, v[242:245], s[6:7]
	s_add_i32 s25, s25, 1
	s_and_b32 s26, s25, 3
	s_cmp_eq_u32 s26, 0
	s_mov_b32 s26, 0xfd001000
	s_cselect_b32 s26, s26, 0x1000000
	s_cselect_b32 s27, -1, 0
	s_add_u32 s6, s6, s26
	s_addc_u32 s7, s7, s27
	s_waitcnt vmcnt(10)
	v_mul_f32_e32 v176, 0x43000000, v176
	v_mul_f32_e32 v177, 0x43000000, v177
	v_mul_f32_e32 v178, 0x43000000, v178
	v_mul_f32_e32 v179, 0x43000000, v179
	ds_write_b128 v210, v[176:179]
	v_mul_f32_e32 v180, 0x43000000, v180
	v_mul_f32_e32 v181, 0x43000000, v181
	v_mul_f32_e32 v182, 0x43000000, v182
	v_mul_f32_e32 v183, 0x43000000, v183
	ds_write_b128 v210, v[180:183] offset:1024
	v_mul_f32_e32 v184, 0x43000000, v184
	v_mul_f32_e32 v185, 0x43000000, v185
	v_mul_f32_e32 v186, 0x43000000, v186
	v_mul_f32_e32 v187, 0x43000000, v187
	ds_write_b128 v210, v[184:187] offset:2048
	v_mul_f32_e32 v188, 0x43000000, v188
	v_mul_f32_e32 v189, 0x43000000, v189
	v_mul_f32_e32 v190, 0x43000000, v190
	v_mul_f32_e32 v191, 0x43000000, v191
	ds_write_b128 v210, v[188:191] offset:3072
	v_mul_f32_e32 v192, 0x43000000, v192
	v_mul_f32_e32 v193, 0x43000000, v193
	v_mul_f32_e32 v194, 0x43000000, v194
	v_mul_f32_e32 v195, 0x43000000, v195
	ds_write_b128 v210, v[192:195] offset:4096
	v_mul_f32_e32 v196, 0x43000000, v196
	v_mul_f32_e32 v197, 0x43000000, v197
	v_mul_f32_e32 v198, 0x43000000, v198
	v_mul_f32_e32 v199, 0x43000000, v199
	ds_write_b128 v210, v[196:199] offset:5120
	v_mul_f32_e32 v200, 0x43000000, v200
	v_mul_f32_e32 v201, 0x43000000, v201
	v_mul_f32_e32 v202, 0x43000000, v202
	v_mul_f32_e32 v203, 0x43000000, v203
	ds_write_b128 v210, v[200:203] offset:6144
	v_mul_f32_e32 v204, 0x43000000, v204
	v_mul_f32_e32 v205, 0x43000000, v205
	v_mul_f32_e32 v206, 0x43000000, v206
	v_mul_f32_e32 v207, 0x43000000, v207
	ds_write_b128 v210, v[204:207] offset:7168
	s_waitcnt lgkmcnt(0)
	s_barrier
; #define GAS __attribute__((address_space(1)))
; #define LAS __attribute__((address_space(3)))
; #define LDS_WAIT() asm volatile("s_waitcnt lgkmcnt(0)" ::: "memory")
;     const int pr = item >> 1, kb = 2 * (pr / nblk) + (item & 1), nb = pr % nblk, k0 = 64 * kb, n0 = 32 * nb;
;     const int nr = n0 + (lane & 31); const int sc = MAP == 1 ? src_col_in(nr) : nr;
;     float v[32];
; #pragma unroll
;     for (int i = 0; i < 32; ++i) v[i] = sc >= 0 ? W[(size_t)(k0 + 2 * i + (lane >> 5)) * Nsrc + sc] : 0.f;
; #pragma unroll
;     for (int i = 0; i < 32; ++i) { const int k = k0 + 2 * i + (lane >> 5); float x = v[i] * wscale; if (KS) x *= (k < ksplit ? ksA[k] : ksB[k - ksplit]); scr[(2 * i + (lane >> 5)) * 33 + (lane & 31)] = x; }
;     LDS_WAIT(); asm volatile("" ::: "memory");
;     const int c = lane & 7;
; #pragma unroll
;     for (int j = 0; j < 4; ++j) { const int n = (lane >> 3) + 8 * j; const LAS float* s = scr + (8 * c) * 33 + n;
;         const unsigned long long o = (unsigned long long)pg8::pk4_fp8(s[0 * 33], s[1 * 33], s[2 * 33], s[3 * 33]) | ((unsigned long long)pg8::pk4_fp8(s[4 * 33], s[5 * 33], s[6 * 33], s[7 * 33]) << 32);
;         *(GAS unsigned long long*)(WT + (size_t)(n0 + n) * K + k0 + 8 * c) = o; }
;     LDS_WAIT(); asm volatile("" ::: "memory");
; }
; __global__ void __launch_bounds__(NWAVES * 64, 2) hybrid_fwd(Args args) {
;     ...
;             p0_transpose_item_f8<false>(args.in[16] + (size_t)l * FF * DM, FF, DM, DM / 32, (unsigned char*)(ws + WS_WDN + l * SZ_WDN), 128.f, args.in[16], args.in[16], 0, scr, r, lane);
	s_mov_b64 s[8:9], s[4:5]
	global_load_dwordx4 v[176:179], v208, s[8:9]
	s_add_u32 s8, s8, 0x8000
	s_addc_u32 s9, s9, 0
	global_load_dwordx4 v[180:183], v208, s[8:9]
	s_add_u32 s8, s8, 0x8000
	s_addc_u32 s9, s9, 0
	global_load_dwordx4 v[184:187], v208, s[8:9]
	s_add_u32 s8, s8, 0x8000
	s_addc_u32 s9, s9, 0
	global_load_dwordx4 v[188:191], v208, s[8:9]
	s_add_u32 s8, s8, 0x8000
	s_addc_u32 s9, s9, 0
	global_load_dwordx4 v[192:195], v208, s[8:9]
	s_add_u32 s8, s8, 0x8000
	s_addc_u32 s9, s9, 0
	global_load_dwordx4 v[196:199], v208, s[8:9]
	s_add_u32 s8, s8, 0x8000
	s_addc_u32 s9, s9, 0
	global_load_dwordx4 v[200:203], v208, s[8:9]
	s_add_u32 s8, s8, 0x8000
	s_addc_u32 s9, s9, 0
	global_load_dwordx4 v[204:207], v208, s[8:9]
	s_add_i32 s24, s24, 1
	s_and_b32 s26, s24, 3
	s_cmp_eq_u32 s26, 0
	s_mov_b32 s26, 0x3ffd000
	s_cselect_b32 s26, s26, 0x1000
	s_add_u32 s4, s4, s26
	s_addc_u32 s5, s5, 0
	ds_read_b32 v226, v212
	ds_read_b32 v227, v212 offset:512
	ds_read_b32 v228, v212 offset:1024
	ds_read_b32 v229, v212 offset:1536
	ds_read_b32 v230, v212 offset:2048
	ds_read_b32 v231, v212 offset:2560
	ds_read_b32 v232, v212 offset:3072
	ds_read_b32 v233, v212 offset:3584
	ds_read_b32 v234, v212 offset:4096
	ds_read_b32 v235, v212 offset:4608
	ds_read_b32 v236, v212 offset:5120
	ds_read_b32 v237, v212 offset:5632
	ds_read_b32 v238, v212 offset:6144
	ds_read_b32 v239, v212 offset:6656
	ds_read_b32 v240, v212 offset:7168
	ds_read_b32 v241, v212 offset:7680
	s_waitcnt lgkmcnt(0)
	v_max_f32_e32 v226, v226, v226
	v_max_f32_e32 v227, v227, v227
	v_max_f32_e32 v228, v228, v228
	v_max_f32_e32 v229, v229, v229
	v_max_f32_e32 v230, v230, v230
	v_max_f32_e32 v231, v231, v231
	v_max_f32_e32 v232, v232, v232
	v_max_f32_e32 v233, v233, v233
	v_max_f32_e32 v234, v234, v234
	v_max_f32_e32 v235, v235, v235
	v_max_f32_e32 v236, v236, v236
	v_max_f32_e32 v237, v237, v237
	v_max_f32_e32 v238, v238, v238
	v_max_f32_e32 v239, v239, v239
	v_max_f32_e32 v240, v240, v240
	v_max_f32_e32 v241, v241, v241
	v_med3_f32 v226, v226, s44, v246
	v_med3_f32 v227, v227, s44, v246
	v_med3_f32 v228, v228, s44, v246
	v_med3_f32 v229, v229, s44, v246
	v_med3_f32 v230, v230, s44, v246
	v_med3_f32 v231, v231, s44, v246
	v_med3_f32 v232, v232, s44, v246
	v_med3_f32 v233, v233, s44, v246
	v_med3_f32 v234, v234, s44, v246
	v_med3_f32 v235, v235, s44, v246
	v_med3_f32 v236, v236, s44, v246
	v_med3_f32 v237, v237, s44, v246
	v_med3_f32 v238, v238, s44, v246
	v_med3_f32 v239, v239, s44, v246
	v_med3_f32 v240, v240, s44, v246
	v_med3_f32 v241, v241, s44, v246
	v_mov_b32_e32 v242, 0
	v_mov_b32_e32 v243, 0
	v_mov_b32_e32 v244, 0
	v_mov_b32_e32 v245, 0
	v_cvt_pk_fp8_f32 v242, v226, v227
	v_cvt_pk_fp8_f32 v243, v230, v231
	v_cvt_pk_fp8_f32 v244, v234, v235
	v_cvt_pk_fp8_f32 v245, v238, v239
	v_cvt_pk_fp8_f32 v242, v228, v229 op_sel:[0,0,1]
	v_cvt_pk_fp8_f32 v243, v232, v233 op_sel:[0,0,1]
	v_cvt_pk_fp8_f32 v244, v236, v237 op_sel:[0,0,1]
	v_cvt_pk_fp8_f32 v245, v240, v241 op_sel:[0,0,1]
	s_nop 0
	global_store_dwordx4 v215, v[242:245], s[6:7]
	ds_read_b32 v226, v214
	ds_read_b32 v227, v214 offset:512
	ds_read_b32 v228, v214 offset:1024
	ds_read_b32 v229, v214 offset:1536
	ds_read_b32 v230, v214 offset:2048
	ds_read_b32 v231, v214 offset:2560
	ds_read_b32 v232, v214 offset:3072
	ds_read_b32 v233, v214 offset:3584
	ds_read_b32 v234, v214 offset:4096
	ds_read_b32 v235, v214 offset:4608
	ds_read_b32 v236, v214 offset:5120
	ds_read_b32 v237, v214 offset:5632
	ds_read_b32 v238, v214 offset:6144
	ds_read_b32 v239, v214 offset:6656
	ds_read_b32 v240, v214 offset:7168
	ds_read_b32 v241, v214 offset:7680
	s_waitcnt lgkmcnt(0)
	v_max_f32_e32 v226, v226, v226
	v_max_f32_e32 v227, v227, v227
	v_max_f32_e32 v228, v228, v228
	v_max_f32_e32 v229, v229, v229
	v_max_f32_e32 v230, v230, v230
	v_max_f32_e32 v231, v231, v231
	v_max_f32_e32 v232, v232, v232
	v_max_f32_e32 v233, v233, v233
	v_max_f32_e32 v234, v234, v234
	v_max_f32_e32 v235, v235, v235
	v_max_f32_e32 v236, v236, v236
	v_max_f32_e32 v237, v237, v237
	v_max_f32_e32 v238, v238, v238
	v_max_f32_e32 v239, v239, v239
	v_max_f32_e32 v240, v240, v240
	v_max_f32_e32 v241, v241, v241
	v_med3_f32 v226, v226, s44, v246
	v_med3_f32 v227, v227, s44, v246
	v_med3_f32 v228, v228, s44, v246
	v_med3_f32 v229, v229, s44, v246
	v_med3_f32 v230, v230, s44, v246
	v_med3_f32 v231, v231, s44, v246
	v_med3_f32 v232, v232, s44, v246
	v_med3_f32 v233, v233, s44, v246
	v_med3_f32 v234, v234, s44, v246
	v_med3_f32 v235, v235, s44, v246
	v_med3_f32 v236, v236, s44, v246
	v_med3_f32 v237, v237, s44, v246
	v_med3_f32 v238, v238, s44, v246
	v_med3_f32 v239, v239, s44, v246
	v_med3_f32 v240, v240, s44, v246
	v_med3_f32 v241, v241, s44, v246
	v_mov_b32_e32 v242, 0
	v_mov_b32_e32 v243, 0
	v_mov_b32_e32 v244, 0
	v_mov_b32_e32 v245, 0
	v_cvt_pk_fp8_f32 v242, v226, v227
	v_cvt_pk_fp8_f32 v243, v230, v231
	v_cvt_pk_fp8_f32 v244, v234, v235
	v_cvt_pk_fp8_f32 v245, v238, v239
	v_cvt_pk_fp8_f32 v242, v228, v229 op_sel:[0,0,1]
	v_cvt_pk_fp8_f32 v243, v232, v233 op_sel:[0,0,1]
	v_cvt_pk_fp8_f32 v244, v236, v237 op_sel:[0,0,1]
	v_cvt_pk_fp8_f32 v245, v240, v241 op_sel:[0,0,1]
	s_nop 0
	global_store_dwordx4 v216, v[242:245], s[6:7]
	s_add_i32 s25, s25, 1
	s_and_b32 s26, s25, 3
	s_cmp_eq_u32 s26, 0
	s_mov_b32 s26, 0xfd001000
	s_cselect_b32 s26, s26, 0x1000000
	s_cselect_b32 s27, -1, 0
	s_add_u32 s6, s6, s26
	s_addc_u32 s7, s7, s27
	s_mov_b32 s12, 6
; #define GAS __attribute__((address_space(1)))
; #define LAS __attribute__((address_space(3)))
; #define LDS_WAIT() asm volatile("s_waitcnt lgkmcnt(0)" ::: "memory")
;     const int pr = item >> 1, kb = 2 * (pr / nblk) + (item & 1), nb = pr % nblk, k0 = 64 * kb, n0 = 32 * nb;
;     const int nr = n0 + (lane & 31); const int sc = MAP == 1 ? src_col_in(nr) : nr;
;     float v[32];
; #pragma unroll
;     for (int i = 0; i < 32; ++i) v[i] = sc >= 0 ? W[(size_t)(k0 + 2 * i + (lane >> 5)) * Nsrc + sc] : 0.f;
; #pragma unroll
;     for (int i = 0; i < 32; ++i) { const int k = k0 + 2 * i + (lane >> 5); float x = v[i] * wscale; if (KS) x *= (k < ksplit ? ksA[k] : ksB[k - ksplit]); scr[(2 * i + (lane >> 5)) * 33 + (lane & 31)] = x; }
;     LDS_WAIT(); asm volatile("" ::: "memory");
;     const int c = lane & 7;
; #pragma unroll
;     for (int j = 0; j < 4; ++j) { const int n = (lane >> 3) + 8 * j; const LAS float* s = scr + (8 * c) * 33 + n;
;         const unsigned long long o = (unsigned long long)pg8::pk4_fp8(s[0 * 33], s[1 * 33], s[2 * 33], s[3 * 33]) | ((unsigned long long)pg8::pk4_fp8(s[4 * 33], s[5 * 33], s[6 * 33], s[7 * 33]) << 32);
;         *(GAS unsigned long long*)(WT + (size_t)(n0 + n) * K + k0 + 8 * c) = o; }
;     LDS_WAIT(); asm volatile("" ::: "memory");
; }
; __global__ void __launch_bounds__(NWAVES * 64, 2) hybrid_fwd(Args args) {
;     ...
;             p0_transpose_item_f8<false>(args.in[16] + (size_t)l * FF * DM, FF, DM, DM / 32, (unsigned char*)(ws + WS_WDN + l * SZ_WDN), 128.f, args.in[16], args.in[16], 0, scr, r, lane);
.Lco_wdn_loop:
	s_waitcnt vmcnt(12)
	v_mul_f32_e32 v144, 0x43000000, v144
	v_mul_f32_e32 v145, 0x43000000, v145
	v_mul_f32_e32 v146, 0x43000000, v146
	v_mul_f32_e32 v147, 0x43000000, v147
	ds_write_b128 v209, v[144:147]
	v_mul_f32_e32 v148, 0x43000000, v148
	v_mul_f32_e32 v149, 0x43000000, v149
	v_mul_f32_e32 v150, 0x43000000, v150
	v_mul_f32_e32 v151, 0x43000000, v151
	ds_write_b128 v209, v[148:151] offset:1024
	v_mul_f32_e32 v152, 0x43000000, v152
	v_mul_f32_e32 v153, 0x43000000, v153
	v_mul_f32_e32 v154, 0x43000000, v154
	v_mul_f32_e32 v155, 0x43000000, v155
	ds_write_b128 v209, v[152:155] offset:2048
	v_mul_f32_e32 v156, 0x43000000, v156
	v_mul_f32_e32 v157, 0x43000000, v157
	v_mul_f32_e32 v158, 0x43000000, v158
	v_mul_f32_e32 v159, 0x43000000, v159
	ds_write_b128 v209, v[156:159] offset:3072
	v_mul_f32_e32 v160, 0x43000000, v160
	v_mul_f32_e32 v161, 0x43000000, v161
	v_mul_f32_e32 v162, 0x43000000, v162
	v_mul_f32_e32 v163, 0x43000000, v163
	ds_write_b128 v209, v[160:163] offset:4096
	v_mul_f32_e32 v164, 0x43000000, v164
	v_mul_f32_e32 v165, 0x43000000, v165
	v_mul_f32_e32 v166, 0x43000000, v166
	v_mul_f32_e32 v167, 0x43000000, v167
	ds_write_b128 v209, v[164:167] offset:5120
	v_mul_f32_e32 v168, 0x43000000, v168
	v_mul_f32_e32 v169, 0x43000000, v169
	v_mul_f32_e32 v170, 0x43000000, v170
	v_mul_f32_e32 v171, 0x43000000, v171
	ds_write_b128 v209, v[168:171] offset:6144
	v_mul_f32_e32 v172, 0x43000000, v172
	v_mul_f32_e32 v173, 0x43000000, v173
	v_mul_f32_e32 v174, 0x43000000, v174
	v_mul_f32_e32 v175, 0x43000000, v175
	ds_write_b128 v209, v[172:175] offset:7168
	s_waitcnt lgkmcnt(0)
	s_barrier
	s_mov_b64 s[8:9], s[4:5]
	global_load_dwordx4 v[144:147], v208, s[8:9]
	s_add_u32 s8, s8, 0x8000
	s_addc_u32 s9, s9, 0
	global_load_dwordx4 v[148:151], v208, s[8:9]
	s_add_u32 s8, s8, 0x8000
	s_addc_u32 s9, s9, 0
	global_load_dwordx4 v[152:155], v208, s[8:9]
	s_add_u32 s8, s8, 0x8000
	s_addc_u32 s9, s9, 0
	global_load_dwordx4 v[156:159], v208, s[8:9]
	s_add_u32 s8, s8, 0x8000
	s_addc_u32 s9, s9, 0
	global_load_dwordx4 v[160:163], v208, s[8:9]
	s_add_u32 s8, s8, 0x8000
	s_addc_u32 s9, s9, 0
	global_load_dwordx4 v[164:167], v208, s[8:9]
	s_add_u32 s8, s8, 0x8000
	s_addc_u32 s9, s9, 0
	global_load_dwordx4 v[168:171], v208, s[8:9]
	s_add_u32 s8, s8, 0x8000
	s_addc_u32 s9, s9, 0
	global_load_dwordx4 v[172:175], v208, s[8:9]
	s_add_i32 s24, s24, 1
	s_and_b32 s26, s24, 3
	s_cmp_eq_u32 s26, 0
	s_mov_b32 s26, 0x3ffd000
	s_cselect_b32 s26, s26, 0x1000
	s_add_u32 s4, s4, s26
	s_addc_u32 s5, s5, 0
	ds_read_b32 v226, v211
	ds_read_b32 v227, v211 offset:512
	ds_read_b32 v228, v211 offset:1024
	ds_read_b32 v229, v211 offset:1536
	ds_read_b32 v230, v211 offset:2048
	ds_read_b32 v231, v211 offset:2560
	ds_read_b32 v232, v211 offset:3072
	ds_read_b32 v233, v211 offset:3584
	ds_read_b32 v234, v211 offset:4096
	ds_read_b32 v235, v211 offset:4608
	ds_read_b32 v236, v211 offset:5120
	ds_read_b32 v237, v211 offset:5632
	ds_read_b32 v238, v211 offset:6144
	ds_read_b32 v239, v211 offset:6656
	ds_read_b32 v240, v211 offset:7168
	ds_read_b32 v241, v211 offset:7680
	s_waitcnt lgkmcnt(0)
	v_max_f32_e32 v226, v226, v226
	v_max_f32_e32 v227, v227, v227
	v_max_f32_e32 v228, v228, v228
	v_max_f32_e32 v229, v229, v229
	v_max_f32_e32 v230, v230, v230
	v_max_f32_e32 v231, v231, v231
	v_max_f32_e32 v232, v232, v232
	v_max_f32_e32 v233, v233, v233
	v_max_f32_e32 v234, v234, v234
	v_max_f32_e32 v235, v235, v235
	v_max_f32_e32 v236, v236, v236
	v_max_f32_e32 v237, v237, v237
	v_max_f32_e32 v238, v238, v238
	v_max_f32_e32 v239, v239, v239
	v_max_f32_e32 v240, v240, v240
	v_max_f32_e32 v241, v241, v241
	v_med3_f32 v226, v226, s44, v246
	v_med3_f32 v227, v227, s44, v246
	v_med3_f32 v228, v228, s44, v246
	v_med3_f32 v229, v229, s44, v246
	v_med3_f32 v230, v230, s44, v246
	v_med3_f32 v231, v231, s44, v246
	v_med3_f32 v232, v232, s44, v246
	v_med3_f32 v233, v233, s44, v246
	v_med3_f32 v234, v234, s44, v246
	v_med3_f32 v235, v235, s44, v246
	v_med3_f32 v236, v236, s44, v246
	v_med3_f32 v237, v237, s44, v246
	v_med3_f32 v238, v238, s44, v246
	v_med3_f32 v239, v239, s44, v246
	v_med3_f32 v240, v240, s44, v246
	v_med3_f32 v241, v241, s44, v246
	v_mov_b32_e32 v242, 0
	v_mov_b32_e32 v243, 0
	v_mov_b32_e32 v244, 0
	v_mov_b32_e32 v245, 0
	v_cvt_pk_fp8_f32 v242, v226, v227
	v_cvt_pk_fp8_f32 v243, v230, v231
	v_cvt_pk_fp8_f32 v244, v234, v235
	v_cvt_pk_fp8_f32 v245, v238, v239
	v_cvt_pk_fp8_f32 v242, v228, v229 op_sel:[0,0,1]
	v_cvt_pk_fp8_f32 v243, v232, v233 op_sel:[0,0,1]
	v_cvt_pk_fp8_f32 v244, v236, v237 op_sel:[0,0,1]
	v_cvt_pk_fp8_f32 v245, v240, v241 op_sel:[0,0,1]
	s_nop 0
	global_store_dwordx4 v215, v[242:245], s[6:7]
	ds_read_b32 v226, v213
	ds_read_b32 v227, v213 offset:512
	ds_read_b32 v228, v213 offset:1024
	ds_read_b32 v229, v213 offset:1536
	ds_read_b32 v230, v213 offset:2048
	ds_read_b32 v231, v213 offset:2560
	ds_read_b32 v232, v213 offset:3072
	ds_read_b32 v233, v213 offset:3584
	ds_read_b32 v234, v213 offset:4096
	ds_read_b32 v235, v213 offset:4608
	ds_read_b32 v236, v213 offset:5120
	ds_read_b32 v237, v213 offset:5632
	ds_read_b32 v238, v213 offset:6144
	ds_read_b32 v239, v213 offset:6656
	ds_read_b32 v240, v213 offset:7168
	ds_read_b32 v241, v213 offset:7680
	s_waitcnt lgkmcnt(0)
; #define GAS __attribute__((address_space(1)))
; #define LAS __attribute__((address_space(3)))
; #define LDS_WAIT() asm volatile("s_waitcnt lgkmcnt(0)" ::: "memory")
;     const int pr = item >> 1, kb = 2 * (pr / nblk) + (item & 1), nb = pr % nblk, k0 = 64 * kb, n0 = 32 * nb;
;     const int nr = n0 + (lane & 31); const int sc = MAP == 1 ? src_col_in(nr) : nr;
;     float v[32];
; #pragma unroll
;     for (int i = 0; i < 32; ++i) v[i] = sc >= 0 ? W[(size_t)(k0 + 2 * i + (lane >> 5)) * Nsrc + sc] : 0.f;
; #pragma unroll
;     for (int i = 0; i < 32; ++i) { const int k = k0 + 2 * i + (lane >> 5); float x = v[i] * wscale; if (KS) x *= (k < ksplit ? ksA[k] : ksB[k - ksplit]); scr[(2 * i + (lane >> 5)) * 33 + (lane & 31)] = x; }
;     LDS_WAIT(); asm volatile("" ::: "memory");
;     const int c = lane & 7;
; #pragma unroll
;     for (int j = 0; j < 4; ++j) { const int n = (lane >> 3) + 8 * j; const LAS float* s = scr + (8 * c) * 33 + n;
;         const unsigned long long o = (unsigned long long)pg8::pk4_fp8(s[0 * 33], s[1 * 33], s[2 * 33], s[3 * 33]) | ((unsigned long long)pg8::pk4_fp8(s[4 * 33], s[5 * 33], s[6 * 33], s[7 * 33]) << 32);
;         *(GAS unsigned long long*)(WT + (size_t)(n0 + n) * K + k0 + 8 * c) = o; }
;     LDS_WAIT(); asm volatile("" ::: "memory");
; }
; __global__ void __launch_bounds__(NWAVES * 64, 2) hybrid_fwd(Args args) {
;     ...
;             p0_transpose_item_f8<false>(args.in[16] + (size_t)l * FF * DM, FF, DM, DM / 32, (unsigned char*)(ws + WS_WDN + l * SZ_WDN), 128.f, args.in[16], args.in[16], 0, scr, r, lane);
	v_max_f32_e32 v226, v226, v226
	v_max_f32_e32 v227, v227, v227
	v_max_f32_e32 v228, v228, v228
	v_max_f32_e32 v229, v229, v229
	v_max_f32_e32 v230, v230, v230
	v_max_f32_e32 v231, v231, v231
	v_max_f32_e32 v232, v232, v232
	v_max_f32_e32 v233, v233, v233
	v_max_f32_e32 v234, v234, v234
	v_max_f32_e32 v235, v235, v235
	v_max_f32_e32 v236, v236, v236
	v_max_f32_e32 v237, v237, v237
	v_max_f32_e32 v238, v238, v238
	v_max_f32_e32 v239, v239, v239
	v_max_f32_e32 v240, v240, v240
	v_max_f32_e32 v241, v241, v241
	v_med3_f32 v226, v226, s44, v246
	v_med3_f32 v227, v227, s44, v246
	v_med3_f32 v228, v228, s44, v246
	v_med3_f32 v229, v229, s44, v246
	v_med3_f32 v230, v230, s44, v246
	v_med3_f32 v231, v231, s44, v246
	v_med3_f32 v232, v232, s44, v246
	v_med3_f32 v233, v233, s44, v246
	v_med3_f32 v234, v234, s44, v246
	v_med3_f32 v235, v235, s44, v246
	v_med3_f32 v236, v236, s44, v246
	v_med3_f32 v237, v237, s44, v246
	v_med3_f32 v238, v238, s44, v246
	v_med3_f32 v239, v239, s44, v246
	v_med3_f32 v240, v240, s44, v246
	v_med3_f32 v241, v241, s44, v246
	v_mov_b32_e32 v242, 0
	v_mov_b32_e32 v243, 0
	v_mov_b32_e32 v244, 0
	v_mov_b32_e32 v245, 0
	v_cvt_pk_fp8_f32 v242, v226, v227
	v_cvt_pk_fp8_f32 v243, v230, v231
	v_cvt_pk_fp8_f32 v244, v234, v235
	v_cvt_pk_fp8_f32 v245, v238, v239
	v_cvt_pk_fp8_f32 v242, v228, v229 op_sel:[0,0,1]
	v_cvt_pk_fp8_f32 v243, v232, v233 op_sel:[0,0,1]
	v_cvt_pk_fp8_f32 v244, v236, v237 op_sel:[0,0,1]
	v_cvt_pk_fp8_f32 v245, v240, v241 op_sel:[0,0,1]
	s_nop 0
	global_store_dwordx4 v216, v[242:245], s[6:7]
	s_add_i32 s25, s25, 1
	s_and_b32 s26, s25, 3
	s_cmp_eq_u32 s26, 0
	s_mov_b32 s26, 0xfd001000
	s_cselect_b32 s26, s26, 0x1000000
	s_cselect_b32 s27, -1, 0
	s_add_u32 s6, s6, s26
	s_addc_u32 s7, s7, s27
	s_waitcnt vmcnt(12)
	v_mul_f32_e32 v176, 0x43000000, v176
	v_mul_f32_e32 v177, 0x43000000, v177
	v_mul_f32_e32 v178, 0x43000000, v178
	v_mul_f32_e32 v179, 0x43000000, v179
	ds_write_b128 v210, v[176:179]
	v_mul_f32_e32 v180, 0x43000000, v180
	v_mul_f32_e32 v181, 0x43000000, v181
	v_mul_f32_e32 v182, 0x43000000, v182
	v_mul_f32_e32 v183, 0x43000000, v183
	ds_write_b128 v210, v[180:183] offset:1024
	v_mul_f32_e32 v184, 0x43000000, v184
	v_mul_f32_e32 v185, 0x43000000, v185
	v_mul_f32_e32 v186, 0x43000000, v186
	v_mul_f32_e32 v187, 0x43000000, v187
	ds_write_b128 v210, v[184:187] offset:2048
	v_mul_f32_e32 v188, 0x43000000, v188
	v_mul_f32_e32 v189, 0x43000000, v189
	v_mul_f32_e32 v190, 0x43000000, v190
	v_mul_f32_e32 v191, 0x43000000, v191
	ds_write_b128 v210, v[188:191] offset:3072
	v_mul_f32_e32 v192, 0x43000000, v192
	v_mul_f32_e32 v193, 0x43000000, v193
	v_mul_f32_e32 v194, 0x43000000, v194
	v_mul_f32_e32 v195, 0x43000000, v195
	ds_write_b128 v210, v[192:195] offset:4096
	v_mul_f32_e32 v196, 0x43000000, v196
	v_mul_f32_e32 v197, 0x43000000, v197
	v_mul_f32_e32 v198, 0x43000000, v198
	v_mul_f32_e32 v199, 0x43000000, v199
	ds_write_b128 v210, v[196:199] offset:5120
	v_mul_f32_e32 v200, 0x43000000, v200
	v_mul_f32_e32 v201, 0x43000000, v201
	v_mul_f32_e32 v202, 0x43000000, v202
	v_mul_f32_e32 v203, 0x43000000, v203
	ds_write_b128 v210, v[200:203] offset:6144
	v_mul_f32_e32 v204, 0x43000000, v204
	v_mul_f32_e32 v205, 0x43000000, v205
	v_mul_f32_e32 v206, 0x43000000, v206
	v_mul_f32_e32 v207, 0x43000000, v207
	ds_write_b128 v210, v[204:207] offset:7168
	s_waitcnt lgkmcnt(0)
	s_barrier
	s_mov_b64 s[8:9], s[4:5]
	global_load_dwordx4 v[176:179], v208, s[8:9]
	s_add_u32 s8, s8, 0x8000
	s_addc_u32 s9, s9, 0
	global_load_dwordx4 v[180:183], v208, s[8:9]
	s_add_u32 s8, s8, 0x8000
	s_addc_u32 s9, s9, 0
	global_load_dwordx4 v[184:187], v208, s[8:9]
	s_add_u32 s8, s8, 0x8000
	s_addc_u32 s9, s9, 0
	global_load_dwordx4 v[188:191], v208, s[8:9]
	s_add_u32 s8, s8, 0x8000
	s_addc_u32 s9, s9, 0
	global_load_dwordx4 v[192:195], v208, s[8:9]
	s_add_u32 s8, s8, 0x8000
	s_addc_u32 s9, s9, 0
	global_load_dwordx4 v[196:199], v208, s[8:9]
	s_add_u32 s8, s8, 0x8000
	s_addc_u32 s9, s9, 0
	global_load_dwordx4 v[200:203], v208, s[8:9]
	s_add_u32 s8, s8, 0x8000
	s_addc_u32 s9, s9, 0
	global_load_dwordx4 v[204:207], v208, s[8:9]
	s_add_i32 s24, s24, 1
	s_and_b32 s26, s24, 3
	s_cmp_eq_u32 s26, 0
	s_mov_b32 s26, 0x3ffd000
	s_cselect_b32 s26, s26, 0x1000
	s_add_u32 s4, s4, s26
	s_addc_u32 s5, s5, 0
	ds_read_b32 v226, v212
	ds_read_b32 v227, v212 offset:512
	ds_read_b32 v228, v212 offset:1024
	ds_read_b32 v229, v212 offset:1536
	ds_read_b32 v230, v212 offset:2048
	ds_read_b32 v231, v212 offset:2560
	ds_read_b32 v232, v212 offset:3072
	ds_read_b32 v233, v212 offset:3584
	ds_read_b32 v234, v212 offset:4096
	ds_read_b32 v235, v212 offset:4608
	ds_read_b32 v236, v212 offset:5120
	ds_read_b32 v237, v212 offset:5632
	ds_read_b32 v238, v212 offset:6144
	ds_read_b32 v239, v212 offset:6656
	ds_read_b32 v240, v212 offset:7168
	ds_read_b32 v241, v212 offset:7680
	s_waitcnt lgkmcnt(0)
; #define GAS __attribute__((address_space(1)))
; #define LAS __attribute__((address_space(3)))
; #define LDS_WAIT() asm volatile("s_waitcnt lgkmcnt(0)" ::: "memory")
;     const int pr = item >> 1, kb = 2 * (pr / nblk) + (item & 1), nb = pr % nblk, k0 = 64 * kb, n0 = 32 * nb;
;     const int nr = n0 + (lane & 31); const int sc = MAP == 1 ? src_col_in(nr) : nr;
;     float v[32];
; #pragma unroll
;     for (int i = 0; i < 32; ++i) v[i] = sc >= 0 ? W[(size_t)(k0 + 2 * i + (lane >> 5)) * Nsrc + sc] : 0.f;
; #pragma unroll
;     for (int i = 0; i < 32; ++i) { const int k = k0 + 2 * i + (lane >> 5); float x = v[i] * wscale; if (KS) x *= (k < ksplit ? ksA[k] : ksB[k - ksplit]); scr[(2 * i + (lane >> 5)) * 33 + (lane & 31)] = x; }
;     LDS_WAIT(); asm volatile("" ::: "memory");
;     const int c = lane & 7;
; #pragma unroll
;     for (int j = 0; j < 4; ++j) { const int n = (lane >> 3) + 8 * j; const LAS float* s = scr + (8 * c) * 33 + n;
;         const unsigned long long o = (unsigned long long)pg8::pk4_fp8(s[0 * 33], s[1 * 33], s[2 * 33], s[3 * 33]) | ((unsigned long long)pg8::pk4_fp8(s[4 * 33], s[5 * 33], s[6 * 33], s[7 * 33]) << 32);
;         *(GAS unsigned long long*)(WT + (size_t)(n0 + n) * K + k0 + 8 * c) = o; }
;     LDS_WAIT(); asm volatile("" ::: "memory");
; }
; __global__ void __launch_bounds__(NWAVES * 64, 2) hybrid_fwd(Args args) {
;     ...
;             p0_transpose_item_f8<false>(args.in[16] + (size_t)l * FF * DM, FF, DM, DM / 32, (unsigned char*)(ws + WS_WDN + l * SZ_WDN), 128.f, args.in[16], args.in[16], 0, scr, r, lane);
	v_max_f32_e32 v226, v226, v226
	v_max_f32_e32 v227, v227, v227
	v_max_f32_e32 v228, v228, v228
	v_max_f32_e32 v229, v229, v229
	v_max_f32_e32 v230, v230, v230
	v_max_f32_e32 v231, v231, v231
	v_max_f32_e32 v232, v232, v232
	v_max_f32_e32 v233, v233, v233
	v_max_f32_e32 v234, v234, v234
	v_max_f32_e32 v235, v235, v235
	v_max_f32_e32 v236, v236, v236
	v_max_f32_e32 v237, v237, v237
	v_max_f32_e32 v238, v238, v238
	v_max_f32_e32 v239, v239, v239
	v_max_f32_e32 v240, v240, v240
	v_max_f32_e32 v241, v241, v241
	v_med3_f32 v226, v226, s44, v246
	v_med3_f32 v227, v227, s44, v246
	v_med3_f32 v228, v228, s44, v246
	v_med3_f32 v229, v229, s44, v246
	v_med3_f32 v230, v230, s44, v246
	v_med3_f32 v231, v231, s44, v246
	v_med3_f32 v232, v232, s44, v246
	v_med3_f32 v233, v233, s44, v246
	v_med3_f32 v234, v234, s44, v246
	v_med3_f32 v235, v235, s44, v246
	v_med3_f32 v236, v236, s44, v246
	v_med3_f32 v237, v237, s44, v246
	v_med3_f32 v238, v238, s44, v246
	v_med3_f32 v239, v239, s44, v246
	v_med3_f32 v240, v240, s44, v246
	v_med3_f32 v241, v241, s44, v246
	v_mov_b32_e32 v242, 0
	v_mov_b32_e32 v243, 0
	v_mov_b32_e32 v244, 0
	v_mov_b32_e32 v245, 0
	v_cvt_pk_fp8_f32 v242, v226, v227
	v_cvt_pk_fp8_f32 v243, v230, v231
	v_cvt_pk_fp8_f32 v244, v234, v235
	v_cvt_pk_fp8_f32 v245, v238, v239
	v_cvt_pk_fp8_f32 v242, v228, v229 op_sel:[0,0,1]
	v_cvt_pk_fp8_f32 v243, v232, v233 op_sel:[0,0,1]
	v_cvt_pk_fp8_f32 v244, v236, v237 op_sel:[0,0,1]
	v_cvt_pk_fp8_f32 v245, v240, v241 op_sel:[0,0,1]
	s_nop 0
	global_store_dwordx4 v215, v[242:245], s[6:7]
	ds_read_b32 v226, v214
	ds_read_b32 v227, v214 offset:512
	ds_read_b32 v228, v214 offset:1024
	ds_read_b32 v229, v214 offset:1536
	ds_read_b32 v230, v214 offset:2048
	ds_read_b32 v231, v214 offset:2560
	ds_read_b32 v232, v214 offset:3072
	ds_read_b32 v233, v214 offset:3584
	ds_read_b32 v234, v214 offset:4096
	ds_read_b32 v235, v214 offset:4608
	ds_read_b32 v236, v214 offset:5120
	ds_read_b32 v237, v214 offset:5632
	ds_read_b32 v238, v214 offset:6144
	ds_read_b32 v239, v214 offset:6656
	ds_read_b32 v240, v214 offset:7168
	ds_read_b32 v241, v214 offset:7680
	s_waitcnt lgkmcnt(0)
	v_max_f32_e32 v226, v226, v226
	v_max_f32_e32 v227, v227, v227
	v_max_f32_e32 v228, v228, v228
	v_max_f32_e32 v229, v229, v229
	v_max_f32_e32 v230, v230, v230
	v_max_f32_e32 v231, v231, v231
	v_max_f32_e32 v232, v232, v232
	v_max_f32_e32 v233, v233, v233
	v_max_f32_e32 v234, v234, v234
	v_max_f32_e32 v235, v235, v235
	v_max_f32_e32 v236, v236, v236
	v_max_f32_e32 v237, v237, v237
	v_max_f32_e32 v238, v238, v238
	v_max_f32_e32 v239, v239, v239
	v_max_f32_e32 v240, v240, v240
	v_max_f32_e32 v241, v241, v241
	v_med3_f32 v226, v226, s44, v246
	v_med3_f32 v227, v227, s44, v246
	v_med3_f32 v228, v228, s44, v246
	v_med3_f32 v229, v229, s44, v246
	v_med3_f32 v230, v230, s44, v246
	v_med3_f32 v231, v231, s44, v246
	v_med3_f32 v232, v232, s44, v246
	v_med3_f32 v233, v233, s44, v246
	v_med3_f32 v234, v234, s44, v246
	v_med3_f32 v235, v235, s44, v246
	v_med3_f32 v236, v236, s44, v246
	v_med3_f32 v237, v237, s44, v246
	v_med3_f32 v238, v238, s44, v246
	v_med3_f32 v239, v239, s44, v246
	v_med3_f32 v240, v240, s44, v246
	v_med3_f32 v241, v241, s44, v246
	v_mov_b32_e32 v242, 0
	v_mov_b32_e32 v243, 0
	v_mov_b32_e32 v244, 0
	v_mov_b32_e32 v245, 0
	v_cvt_pk_fp8_f32 v242, v226, v227
	v_cvt_pk_fp8_f32 v243, v230, v231
	v_cvt_pk_fp8_f32 v244, v234, v235
	v_cvt_pk_fp8_f32 v245, v238, v239
	v_cvt_pk_fp8_f32 v242, v228, v229 op_sel:[0,0,1]
	v_cvt_pk_fp8_f32 v243, v232, v233 op_sel:[0,0,1]
	v_cvt_pk_fp8_f32 v244, v236, v237 op_sel:[0,0,1]
	v_cvt_pk_fp8_f32 v245, v240, v241 op_sel:[0,0,1]
	s_nop 0
	global_store_dwordx4 v216, v[242:245], s[6:7]
	s_add_i32 s25, s25, 1
	s_and_b32 s26, s25, 3
	s_cmp_eq_u32 s26, 0
	s_mov_b32 s26, 0xfd001000
	s_cselect_b32 s26, s26, 0x1000000
	s_cselect_b32 s27, -1, 0
	s_add_u32 s6, s6, s26
	s_addc_u32 s7, s7, s27
	s_sub_i32 s12, s12, 1
	s_cmp_lg_u32 s12, 0
	s_cbranch_scc1 .Lco_wdn_loop
	s_waitcnt vmcnt(12)
	v_mul_f32_e32 v144, 0x43000000, v144
	v_mul_f32_e32 v145, 0x43000000, v145
	v_mul_f32_e32 v146, 0x43000000, v146
	v_mul_f32_e32 v147, 0x43000000, v147
	ds_write_b128 v209, v[144:147]
	v_mul_f32_e32 v148, 0x43000000, v148
	v_mul_f32_e32 v149, 0x43000000, v149
	v_mul_f32_e32 v150, 0x43000000, v150
	v_mul_f32_e32 v151, 0x43000000, v151
	ds_write_b128 v209, v[148:151] offset:1024
	v_mul_f32_e32 v152, 0x43000000, v152
	v_mul_f32_e32 v153, 0x43000000, v153
	v_mul_f32_e32 v154, 0x43000000, v154
	v_mul_f32_e32 v155, 0x43000000, v155
	ds_write_b128 v209, v[152:155] offset:2048
	v_mul_f32_e32 v156, 0x43000000, v156
	v_mul_f32_e32 v157, 0x43000000, v157
	v_mul_f32_e32 v158, 0x43000000, v158
	v_mul_f32_e32 v159, 0x43000000, v159
	ds_write_b128 v209, v[156:159] offset:3072
	v_mul_f32_e32 v160, 0x43000000, v160
	v_mul_f32_e32 v161, 0x43000000, v161
	v_mul_f32_e32 v162, 0x43000000, v162
	v_mul_f32_e32 v163, 0x43000000, v163
	ds_write_b128 v209, v[160:163] offset:4096
	v_mul_f32_e32 v164, 0x43000000, v164
	v_mul_f32_e32 v165, 0x43000000, v165
	v_mul_f32_e32 v166, 0x43000000, v166
	v_mul_f32_e32 v167, 0x43000000, v167
	ds_write_b128 v209, v[164:167] offset:5120
	v_mul_f32_e32 v168, 0x43000000, v168
	v_mul_f32_e32 v169, 0x43000000, v169
	v_mul_f32_e32 v170, 0x43000000, v170
	v_mul_f32_e32 v171, 0x43000000, v171
	ds_write_b128 v209, v[168:171] offset:6144
	v_mul_f32_e32 v172, 0x43000000, v172
	v_mul_f32_e32 v173, 0x43000000, v173
	v_mul_f32_e32 v174, 0x43000000, v174
	v_mul_f32_e32 v175, 0x43000000, v175
	ds_write_b128 v209, v[172:175] offset:7168
	s_waitcnt lgkmcnt(0)
	s_barrier
; #define GAS __attribute__((address_space(1)))
; #define LAS __attribute__((address_space(3)))
; #define LDS_WAIT() asm volatile("s_waitcnt lgkmcnt(0)" ::: "memory")
;     const int pr = item >> 1, kb = 2 * (pr / nblk) + (item & 1), nb = pr % nblk, k0 = 64 * kb, n0 = 32 * nb;
;     const int nr = n0 + (lane & 31); const int sc = MAP == 1 ? src_col_in(nr) : nr;
;     float v[32];
; #pragma unroll
;     for (int i = 0; i < 32; ++i) v[i] = sc >= 0 ? W[(size_t)(k0 + 2 * i + (lane >> 5)) * Nsrc + sc] : 0.f;
; #pragma unroll
;     for (int i = 0; i < 32; ++i) { const int k = k0 + 2 * i + (lane >> 5); float x = v[i] * wscale; if (KS) x *= (k < ksplit ? ksA[k] : ksB[k - ksplit]); scr[(2 * i + (lane >> 5)) * 33 + (lane & 31)] = x; }
;     LDS_WAIT(); asm volatile("" ::: "memory");
;     const int c = lane & 7;
; #pragma unroll
;     for (int j = 0; j < 4; ++j) { const int n = (lane >> 3) + 8 * j; const LAS float* s = scr + (8 * c) * 33 + n;
;         const unsigned long long o = (unsigned long long)pg8::pk4_fp8(s[0 * 33], s[1 * 33], s[2 * 33], s[3 * 33]) | ((unsigned long long)pg8::pk4_fp8(s[4 * 33], s[5 * 33], s[6 * 33], s[7 * 33]) << 32);
;         *(GAS unsigned long long*)(WT + (size_t)(n0 + n) * K + k0 + 8 * c) = o; }
;     LDS_WAIT(); asm volatile("" ::: "memory");
; }
; __global__ void __launch_bounds__(NWAVES * 64, 2) hybrid_fwd(Args args) {
;     ...
;             p0_transpose_item_f8<false>(args.in[16] + (size_t)l * FF * DM, FF, DM, DM / 32, (unsigned char*)(ws + WS_WDN + l * SZ_WDN), 128.f, args.in[16], args.in[16], 0, scr, r, lane);
	ds_read_b32 v226, v211
	ds_read_b32 v227, v211 offset:512
	ds_read_b32 v228, v211 offset:1024
	ds_read_b32 v229, v211 offset:1536
	ds_read_b32 v230, v211 offset:2048
	ds_read_b32 v231, v211 offset:2560
	ds_read_b32 v232, v211 offset:3072
	ds_read_b32 v233, v211 offset:3584
	ds_read_b32 v234, v211 offset:4096
	ds_read_b32 v235, v211 offset:4608
	ds_read_b32 v236, v211 offset:5120
	ds_read_b32 v237, v211 offset:5632
	ds_read_b32 v238, v211 offset:6144
	ds_read_b32 v239, v211 offset:6656
	ds_read_b32 v240, v211 offset:7168
	ds_read_b32 v241, v211 offset:7680
	s_waitcnt lgkmcnt(0)
	v_max_f32_e32 v226, v226, v226
	v_max_f32_e32 v227, v227, v227
	v_max_f32_e32 v228, v228, v228
	v_max_f32_e32 v229, v229, v229
	v_max_f32_e32 v230, v230, v230
	v_max_f32_e32 v231, v231, v231
	v_max_f32_e32 v232, v232, v232
	v_max_f32_e32 v233, v233, v233
	v_max_f32_e32 v234, v234, v234
	v_max_f32_e32 v235, v235, v235
	v_max_f32_e32 v236, v236, v236
	v_max_f32_e32 v237, v237, v237
	v_max_f32_e32 v238, v238, v238
	v_max_f32_e32 v239, v239, v239
	v_max_f32_e32 v240, v240, v240
	v_max_f32_e32 v241, v241, v241
	v_med3_f32 v226, v226, s44, v246
	v_med3_f32 v227, v227, s44, v246
	v_med3_f32 v228, v228, s44, v246
	v_med3_f32 v229, v229, s44, v246
	v_med3_f32 v230, v230, s44, v246
	v_med3_f32 v231, v231, s44, v246
	v_med3_f32 v232, v232, s44, v246
	v_med3_f32 v233, v233, s44, v246
	v_med3_f32 v234, v234, s44, v246
	v_med3_f32 v235, v235, s44, v246
	v_med3_f32 v236, v236, s44, v246
	v_med3_f32 v237, v237, s44, v246
	v_med3_f32 v238, v238, s44, v246
	v_med3_f32 v239, v239, s44, v246
	v_med3_f32 v240, v240, s44, v246
	v_med3_f32 v241, v241, s44, v246
	v_mov_b32_e32 v242, 0
	v_mov_b32_e32 v243, 0
	v_mov_b32_e32 v244, 0
	v_mov_b32_e32 v245, 0
	v_cvt_pk_fp8_f32 v242, v226, v227
	v_cvt_pk_fp8_f32 v243, v230, v231
	v_cvt_pk_fp8_f32 v244, v234, v235
	v_cvt_pk_fp8_f32 v245, v238, v239
	v_cvt_pk_fp8_f32 v242, v228, v229 op_sel:[0,0,1]
	v_cvt_pk_fp8_f32 v243, v232, v233 op_sel:[0,0,1]
	v_cvt_pk_fp8_f32 v244, v236, v237 op_sel:[0,0,1]
	v_cvt_pk_fp8_f32 v245, v240, v241 op_sel:[0,0,1]
	s_nop 0
	global_store_dwordx4 v215, v[242:245], s[6:7]
	ds_read_b32 v226, v213
	ds_read_b32 v227, v213 offset:512
	ds_read_b32 v228, v213 offset:1024
	ds_read_b32 v229, v213 offset:1536
	ds_read_b32 v230, v213 offset:2048
	ds_read_b32 v231, v213 offset:2560
	ds_read_b32 v232, v213 offset:3072
	ds_read_b32 v233, v213 offset:3584
	ds_read_b32 v234, v213 offset:4096
	ds_read_b32 v235, v213 offset:4608
	ds_read_b32 v236, v213 offset:5120
	ds_read_b32 v237, v213 offset:5632
	ds_read_b32 v238, v213 offset:6144
	ds_read_b32 v239, v213 offset:6656
	ds_read_b32 v240, v213 offset:7168
	ds_read_b32 v241, v213 offset:7680
	s_waitcnt lgkmcnt(0)
	v_max_f32_e32 v226, v226, v226
	v_max_f32_e32 v227, v227, v227
	v_max_f32_e32 v228, v228, v228
	v_max_f32_e32 v229, v229, v229
	v_max_f32_e32 v230, v230, v230
	v_max_f32_e32 v231, v231, v231
	v_max_f32_e32 v232, v232, v232
	v_max_f32_e32 v233, v233, v233
	v_max_f32_e32 v234, v234, v234
	v_max_f32_e32 v235, v235, v235
	v_max_f32_e32 v236, v236, v236
	v_max_f32_e32 v237, v237, v237
	v_max_f32_e32 v238, v238, v238
	v_max_f32_e32 v239, v239, v239
	v_max_f32_e32 v240, v240, v240
	v_max_f32_e32 v241, v241, v241
	v_med3_f32 v226, v226, s44, v246
	v_med3_f32 v227, v227, s44, v246
	v_med3_f32 v228, v228, s44, v246
	v_med3_f32 v229, v229, s44, v246
	v_med3_f32 v230, v230, s44, v246
	v_med3_f32 v231, v231, s44, v246
	v_med3_f32 v232, v232, s44, v246
	v_med3_f32 v233, v233, s44, v246
	v_med3_f32 v234, v234, s44, v246
	v_med3_f32 v235, v235, s44, v246
	v_med3_f32 v236, v236, s44, v246
	v_med3_f32 v237, v237, s44, v246
	v_med3_f32 v238, v238, s44, v246
	v_med3_f32 v239, v239, s44, v246
	v_med3_f32 v240, v240, s44, v246
	v_med3_f32 v241, v241, s44, v246
	v_mov_b32_e32 v242, 0
	v_mov_b32_e32 v243, 0
	v_mov_b32_e32 v244, 0
	v_mov_b32_e32 v245, 0
	v_cvt_pk_fp8_f32 v242, v226, v227
	v_cvt_pk_fp8_f32 v243, v230, v231
	v_cvt_pk_fp8_f32 v244, v234, v235
	v_cvt_pk_fp8_f32 v245, v238, v239
	v_cvt_pk_fp8_f32 v242, v228, v229 op_sel:[0,0,1]
	v_cvt_pk_fp8_f32 v243, v232, v233 op_sel:[0,0,1]
	v_cvt_pk_fp8_f32 v244, v236, v237 op_sel:[0,0,1]
	v_cvt_pk_fp8_f32 v245, v240, v241 op_sel:[0,0,1]
	s_nop 0
	global_store_dwordx4 v216, v[242:245], s[6:7]
	s_add_i32 s25, s25, 1
	s_and_b32 s26, s25, 3
	s_cmp_eq_u32 s26, 0
	s_mov_b32 s26, 0xfd001000
	s_cselect_b32 s26, s26, 0x1000000
	s_cselect_b32 s27, -1, 0
	s_add_u32 s6, s6, s26
	s_addc_u32 s7, s7, s27
	s_waitcnt vmcnt(4)
	v_mul_f32_e32 v176, 0x43000000, v176
	v_mul_f32_e32 v177, 0x43000000, v177
	v_mul_f32_e32 v178, 0x43000000, v178
	v_mul_f32_e32 v179, 0x43000000, v179
	ds_write_b128 v210, v[176:179]
	v_mul_f32_e32 v180, 0x43000000, v180
	v_mul_f32_e32 v181, 0x43000000, v181
	v_mul_f32_e32 v182, 0x43000000, v182
	v_mul_f32_e32 v183, 0x43000000, v183
	ds_write_b128 v210, v[180:183] offset:1024
	v_mul_f32_e32 v184, 0x43000000, v184
	v_mul_f32_e32 v185, 0x43000000, v185
	v_mul_f32_e32 v186, 0x43000000, v186
	v_mul_f32_e32 v187, 0x43000000, v187
	ds_write_b128 v210, v[184:187] offset:2048
	v_mul_f32_e32 v188, 0x43000000, v188
	v_mul_f32_e32 v189, 0x43000000, v189
	v_mul_f32_e32 v190, 0x43000000, v190
	v_mul_f32_e32 v191, 0x43000000, v191
	ds_write_b128 v210, v[188:191] offset:3072
	v_mul_f32_e32 v192, 0x43000000, v192
	v_mul_f32_e32 v193, 0x43000000, v193
	v_mul_f32_e32 v194, 0x43000000, v194
	v_mul_f32_e32 v195, 0x43000000, v195
	ds_write_b128 v210, v[192:195] offset:4096
	v_mul_f32_e32 v196, 0x43000000, v196
	v_mul_f32_e32 v197, 0x43000000, v197
	v_mul_f32_e32 v198, 0x43000000, v198
	v_mul_f32_e32 v199, 0x43000000, v199
	ds_write_b128 v210, v[196:199] offset:5120
	v_mul_f32_e32 v200, 0x43000000, v200
	v_mul_f32_e32 v201, 0x43000000, v201
	v_mul_f32_e32 v202, 0x43000000, v202
	v_mul_f32_e32 v203, 0x43000000, v203
	ds_write_b128 v210, v[200:203] offset:6144
	v_mul_f32_e32 v204, 0x43000000, v204
	v_mul_f32_e32 v205, 0x43000000, v205
	v_mul_f32_e32 v206, 0x43000000, v206
	v_mul_f32_e32 v207, 0x43000000, v207
	ds_write_b128 v210, v[204:207] offset:7168
	s_waitcnt lgkmcnt(0)
	s_barrier
; #define GAS __attribute__((address_space(1)))
; #define LAS __attribute__((address_space(3)))
; #define LDS_WAIT() asm volatile("s_waitcnt lgkmcnt(0)" ::: "memory")
;     const int pr = item >> 1, kb = 2 * (pr / nblk) + (item & 1), nb = pr % nblk, k0 = 64 * kb, n0 = 32 * nb;
;     const int nr = n0 + (lane & 31); const int sc = MAP == 1 ? src_col_in(nr) : nr;
;     float v[32];
; #pragma unroll
;     for (int i = 0; i < 32; ++i) v[i] = sc >= 0 ? W[(size_t)(k0 + 2 * i + (lane >> 5)) * Nsrc + sc] : 0.f;
; #pragma unroll
;     for (int i = 0; i < 32; ++i) { const int k = k0 + 2 * i + (lane >> 5); float x = v[i] * wscale; if (KS) x *= (k < ksplit ? ksA[k] : ksB[k - ksplit]); scr[(2 * i + (lane >> 5)) * 33 + (lane & 31)] = x; }
;     LDS_WAIT(); asm volatile("" ::: "memory");
;     const int c = lane & 7;
; #pragma unroll
;     for (int j = 0; j < 4; ++j) { const int n = (lane >> 3) + 8 * j; const LAS float* s = scr + (8 * c) * 33 + n;
;         const unsigned long long o = (unsigned long long)pg8::pk4_fp8(s[0 * 33], s[1 * 33], s[2 * 33], s[3 * 33]) | ((unsigned long long)pg8::pk4_fp8(s[4 * 33], s[5 * 33], s[6 * 33], s[7 * 33]) << 32);
;         *(GAS unsigned long long*)(WT + (size_t)(n0 + n) * K + k0 + 8 * c) = o; }
;     LDS_WAIT(); asm volatile("" ::: "memory");
; }
; __global__ void __launch_bounds__(NWAVES * 64, 2) hybrid_fwd(Args args) {
;     ...
;             p0_transpose_item_f8<false>(args.in[16] + (size_t)l * FF * DM, FF, DM, DM / 32, (unsigned char*)(ws + WS_WDN + l * SZ_WDN), 128.f, args.in[16], args.in[16], 0, scr, r, lane);
	ds_read_b32 v226, v212
	ds_read_b32 v227, v212 offset:512
	ds_read_b32 v228, v212 offset:1024
	ds_read_b32 v229, v212 offset:1536
	ds_read_b32 v230, v212 offset:2048
	ds_read_b32 v231, v212 offset:2560
	ds_read_b32 v232, v212 offset:3072
	ds_read_b32 v233, v212 offset:3584
	ds_read_b32 v234, v212 offset:4096
	ds_read_b32 v235, v212 offset:4608
	ds_read_b32 v236, v212 offset:5120
	ds_read_b32 v237, v212 offset:5632
	ds_read_b32 v238, v212 offset:6144
	ds_read_b32 v239, v212 offset:6656
	ds_read_b32 v240, v212 offset:7168
	ds_read_b32 v241, v212 offset:7680
	s_waitcnt lgkmcnt(0)
	v_max_f32_e32 v226, v226, v226
	v_max_f32_e32 v227, v227, v227
	v_max_f32_e32 v228, v228, v228
	v_max_f32_e32 v229, v229, v229
	v_max_f32_e32 v230, v230, v230
	v_max_f32_e32 v231, v231, v231
	v_max_f32_e32 v232, v232, v232
	v_max_f32_e32 v233, v233, v233
	v_max_f32_e32 v234, v234, v234
	v_max_f32_e32 v235, v235, v235
	v_max_f32_e32 v236, v236, v236
	v_max_f32_e32 v237, v237, v237
	v_max_f32_e32 v238, v238, v238
	v_max_f32_e32 v239, v239, v239
	v_max_f32_e32 v240, v240, v240
	v_max_f32_e32 v241, v241, v241
	v_med3_f32 v226, v226, s44, v246
	v_med3_f32 v227, v227, s44, v246
	v_med3_f32 v228, v228, s44, v246
	v_med3_f32 v229, v229, s44, v246
	v_med3_f32 v230, v230, s44, v246
	v_med3_f32 v231, v231, s44, v246
	v_med3_f32 v232, v232, s44, v246
	v_med3_f32 v233, v233, s44, v246
	v_med3_f32 v234, v234, s44, v246
	v_med3_f32 v235, v235, s44, v246
	v_med3_f32 v236, v236, s44, v246
	v_med3_f32 v237, v237, s44, v246
	v_med3_f32 v238, v238, s44, v246
	v_med3_f32 v239, v239, s44, v246
	v_med3_f32 v240, v240, s44, v246
	v_med3_f32 v241, v241, s44, v246
	v_mov_b32_e32 v242, 0
	v_mov_b32_e32 v243, 0
	v_mov_b32_e32 v244, 0
	v_mov_b32_e32 v245, 0
	v_cvt_pk_fp8_f32 v242, v226, v227
	v_cvt_pk_fp8_f32 v243, v230, v231
	v_cvt_pk_fp8_f32 v244, v234, v235
	v_cvt_pk_fp8_f32 v245, v238, v239
	v_cvt_pk_fp8_f32 v242, v228, v229 op_sel:[0,0,1]
	v_cvt_pk_fp8_f32 v243, v232, v233 op_sel:[0,0,1]
	v_cvt_pk_fp8_f32 v244, v236, v237 op_sel:[0,0,1]
	v_cvt_pk_fp8_f32 v245, v240, v241 op_sel:[0,0,1]
	s_nop 0
	global_store_dwordx4 v215, v[242:245], s[6:7]
	ds_read_b32 v226, v214
	ds_read_b32 v227, v214 offset:512
	ds_read_b32 v228, v214 offset:1024
	ds_read_b32 v229, v214 offset:1536
	ds_read_b32 v230, v214 offset:2048
	ds_read_b32 v231, v214 offset:2560
	ds_read_b32 v232, v214 offset:3072
	ds_read_b32 v233, v214 offset:3584
	ds_read_b32 v234, v214 offset:4096
	ds_read_b32 v235, v214 offset:4608
	ds_read_b32 v236, v214 offset:5120
	ds_read_b32 v237, v214 offset:5632
	ds_read_b32 v238, v214 offset:6144
	ds_read_b32 v239, v214 offset:6656
	ds_read_b32 v240, v214 offset:7168
	ds_read_b32 v241, v214 offset:7680
	s_waitcnt lgkmcnt(0)
	v_max_f32_e32 v226, v226, v226
	v_max_f32_e32 v227, v227, v227
	v_max_f32_e32 v228, v228, v228
	v_max_f32_e32 v229, v229, v229
	v_max_f32_e32 v230, v230, v230
	v_max_f32_e32 v231, v231, v231
	v_max_f32_e32 v232, v232, v232
	v_max_f32_e32 v233, v233, v233
	v_max_f32_e32 v234, v234, v234
	v_max_f32_e32 v235, v235, v235
	v_max_f32_e32 v236, v236, v236
	v_max_f32_e32 v237, v237, v237
	v_max_f32_e32 v238, v238, v238
	v_max_f32_e32 v239, v239, v239
	v_max_f32_e32 v240, v240, v240
	v_max_f32_e32 v241, v241, v241
	v_med3_f32 v226, v226, s44, v246
	v_med3_f32 v227, v227, s44, v246
	v_med3_f32 v228, v228, s44, v246
	v_med3_f32 v229, v229, s44, v246
	v_med3_f32 v230, v230, s44, v246
	v_med3_f32 v231, v231, s44, v246
	v_med3_f32 v232, v232, s44, v246
	v_med3_f32 v233, v233, s44, v246
	v_med3_f32 v234, v234, s44, v246
	v_med3_f32 v235, v235, s44, v246
	v_med3_f32 v236, v236, s44, v246
	v_med3_f32 v237, v237, s44, v246
	v_med3_f32 v238, v238, s44, v246
	v_med3_f32 v239, v239, s44, v246
	v_med3_f32 v240, v240, s44, v246
	v_med3_f32 v241, v241, s44, v246
	v_mov_b32_e32 v242, 0
	v_mov_b32_e32 v243, 0
	v_mov_b32_e32 v244, 0
	v_mov_b32_e32 v245, 0
	v_cvt_pk_fp8_f32 v242, v226, v227
	v_cvt_pk_fp8_f32 v243, v230, v231
	v_cvt_pk_fp8_f32 v244, v234, v235
	v_cvt_pk_fp8_f32 v245, v238, v239
	v_cvt_pk_fp8_f32 v242, v228, v229 op_sel:[0,0,1]
	v_cvt_pk_fp8_f32 v243, v232, v233 op_sel:[0,0,1]
	v_cvt_pk_fp8_f32 v244, v236, v237 op_sel:[0,0,1]
	v_cvt_pk_fp8_f32 v245, v240, v241 op_sel:[0,0,1]
	s_nop 0
	global_store_dwordx4 v216, v[242:245], s[6:7]
	s_add_i32 s25, s25, 1
	s_and_b32 s26, s25, 3
	s_cmp_eq_u32 s26, 0
	s_mov_b32 s26, 0xfd001000
	s_cselect_b32 s26, s26, 0x1000000
	s_cselect_b32 s27, -1, 0
	s_add_u32 s6, s6, s26
	s_addc_u32 s7, s7, s27
	s_add_u32 s16, s16, 0x10000000
	s_addc_u32 s17, s17, 0
	s_add_u32 s18, s18, 0x8000000
	s_addc_u32 s19, s19, 0
	s_add_i32 s13, s13, 1
	s_cmp_lg_u32 s13, 2
	s_cbranch_scc1 .Lco_wdn_layer
; __global__ void __launch_bounds__(NWAVES * 64, 2) hybrid_fwd(Args args) {
;     ...
;         for (int rep = 0; rep < REP_PRO; ++rep)
;         for (int it = gw; it < DEPTH * I_L; it += NGW) {
;             const int l = it / I_L; int r = it % I_L;
;             if (r < I_IN) { if (l >= PROJ_F8_FROM) p0_transpose_item_f8<true, 1>(args.in[2] + (size_t)l * DM * NSRC, DM, NSRC, NPROJ / 32, (unsigned char*)(ws + WS_WIN + l * SZ_WIN), WUP8_SCALE, args.in[1] + l * DM, args.in[1] + l * DM, DM, scr, r, lane);
;                 else p0_transpose_item<1, true>(args.in[2] + (size_t)l * DM * NSRC, DM, NSRC, NPROJ / 32, (bf16*)(ws + WS_WIN + l * SZ_WIN), args.in[1] + l * DM, args.in[1] + l * DM, DM, scr, r, lane); continue; } r -= I_IN;
;             if (r < I_O) { if (l >= WO_F8_FROM) p0_transpose_item_f8<true>(args.in[13] + (size_t)l * DM * DM, DM, DM, DM / 32, (unsigned char*)(ws + WS_WO + l * SZ_WO), 64.f, args.in[6] + l * 2048, args.in[12] + l * 2048, 2048, scr, r, lane);
;                 else p0_transpose_item<0, true>(args.in[13] + (size_t)l * DM * DM, DM, DM, DM / 32, (bf16*)(ws + WS_WO + l * SZ_WO), args.in[6] + l * 2048, args.in[12] + l * 2048, 2048, scr, r, lane); continue; } r -= I_O;
;             if (r < I_UP) { p0_transpose_item_f8<true>(args.in[15] + (size_t)l * DM * FF, DM, FF, FF / 32, (unsigned char*)(ws + WS_WUP + l * SZ_WUP), WUP8_SCALE, args.in[14] + l * DM, args.in[14] + l * DM, DM, scr, r, lane); continue; } r -= I_UP;
;             p0_transpose_item_f8<false>(args.in[16] + (size_t)l * FF * DM, FF, DM, DM / 32, (unsigned char*)(ws + WS_WDN + l * SZ_WDN), 128.f, args.in[16], args.in[16], 0, scr, r, lane);
;         }
	s_waitcnt lgkmcnt(0)
	s_barrier
	v_readlane_b32 s12, v253, 35
	v_readlane_b32 s18, v253, 41
	v_readlane_b32 s19, v253, 42
	s_add_u32 s81, s18, 0x1f600000
	s_addc_u32 s94, s19, 0
	s_add_u32 s24, s18, 0xf600000
	v_or_b32_e32 v2, 2, v6
	v_mov_b32_e32 v3, 0x630
	v_readlane_b32 s13, v253, 36
	v_readlane_b32 s14, v253, 37
	v_readlane_b32 s15, v253, 38
	s_addc_u32 s25, s19, 0
	v_mad_u32_u24 v58, v2, s0, v3
	v_mov_b32_e32 v3, 0xc60
	s_add_u32 s26, s18, 0xb600000
	v_mad_u32_u24 v59, v2, s0, v3
	v_readlane_b32 s0, v253, 19
	s_addc_u32 s27, s19, 0
	v_readlane_b32 s2, v253, 21
	v_readlane_b32 s10, v253, 29
	v_readlane_b32 s3, v253, 22
	v_readlane_b32 s11, v253, 30
	s_add_u32 s2, s10, 0x4000000
	v_readlane_b32 s40, v253, 3
	s_addc_u32 s3, s11, 0
	v_readlane_b32 s52, v253, 15
	v_readlane_b32 s53, v253, 16
	s_add_u32 s22, s52, 0x2000
	v_readlane_b32 s8, v253, 27
	s_addc_u32 s23, s53, 0
	v_readlane_b32 s9, v253, 28
	s_add_u32 s84, s8, 0x2000
	s_addc_u32 s85, s9, 0
	s_add_u32 s33, s18, 0x200000
	v_readlane_b32 s44, v253, 7
	s_addc_u32 s38, s19, 0
	v_mov_b32_e32 v9, v11
	v_readlane_b32 s1, v253, 20
	v_readlane_b32 s45, v253, 8
	s_add_u32 s86, s44, 0xb140000
	v_mul_u32_u24_e32 v57, 0x84, v2
	v_readlane_b32 s42, v253, 5
	v_lshl_add_u64 v[2:3], s[18:19], 0, v[8:9]
	s_mov_b64 s[0:1], 0xd600000
	s_addc_u32 s87, s45, 0
	v_readlane_b32 s12, v253, 31
	v_readlane_b32 s13, v253, 32
	v_readlane_b32 s14, v253, 33
	v_readlane_b32 s15, v253, 34
	v_readlane_b32 s43, v253, 6
	v_readlane_b32 s54, v253, 17
	v_readlane_b32 s55, v253, 18
	v_lshl_add_u64 v[12:13], v[2:3], 0, s[0:1]
	s_add_u32 s88, s42, 0x4000
	s_mov_b64 s[0:1], 0x5c00000
	v_readlane_b32 s41, v253, 4
	v_readlane_b32 s46, v253, 9
	v_readlane_b32 s47, v253, 10
	v_readlane_b32 s48, v253, 11
	v_readlane_b32 s49, v253, 12
	v_readlane_b32 s50, v253, 13
	s_addc_u32 s89, s43, 0
	v_lshlrev_b32_e32 v4, 6, v18
	v_lshl_add_u64 v[14:15], v[2:3], 0, s[0:1]
	s_lshl_b32 s0, s80, 5
	s_movk_i32 s12, 0xe000
	s_movk_i32 s14, 0xe008
	s_movk_i32 s18, 0xe010
	s_movk_i32 s78, 0xe018
	s_movk_i32 s92, 0xe0d0
	s_movk_i32 s28, 0xe0d8
	s_movk_i32 s34, 0xe0e0
	s_movk_i32 s52, 0xe0e8
	s_movk_i32 s54, 0xe0f0
	s_movk_i32 s56, 0xe0f8
	v_or_b32_e32 v26, 0x2000, v18
	v_or_b32_e32 v27, 0x4000, v18
	v_or_b32_e32 v28, 0x6000, v18
	v_or_b32_e32 v29, 0x8000, v18
	v_or_b32_e32 v30, 0xa000, v18
	v_or_b32_e32 v31, 0xc000, v18
	v_or_b32_e32 v32, 0xe000, v18
	v_or_b32_e32 v33, 0x10000, v18
	v_or_b32_e32 v34, 0x12000, v18
	v_or_b32_e32 v35, 0x14000, v18
	v_or_b32_e32 v36, 0x16000, v18
	v_or_b32_e32 v37, 0x18000, v18
	v_or_b32_e32 v38, 0x1a000, v18
	v_or_b32_e32 v39, 0x1c000, v18
	v_or_b32_e32 v40, 0x1e000, v18
	v_or_b32_e32 v41, 0x20000, v18
	v_or_b32_e32 v42, 0x22000, v18
	v_or_b32_e32 v43, 0x24000, v18
	v_or_b32_e32 v44, 0x26000, v18
	v_or_b32_e32 v45, 0x28000, v18
	v_or_b32_e32 v46, 0x2a000, v18
	v_or_b32_e32 v47, 0x2c000, v18
	v_or_b32_e32 v48, 0x2e000, v18
	v_or_b32_e32 v49, 0x30000, v18
	v_or_b32_e32 v50, 0x32000, v18
	v_or_b32_e32 v51, 0x34000, v18
	v_or_b32_e32 v52, 0x36000, v18
	v_or_b32_e32 v53, 0x38000, v18
	v_or_b32_e32 v54, 0x3a000, v18
	v_or_b32_e32 v55, 0x3c000, v18
	v_or_b32_e32 v56, 0x3e000, v18
	v_and_b32_e32 v60, 64, v4
	v_mov_b32_e32 v7, v11
	s_lshl_b32 s39, s80, 6
	s_add_i32 s40, s0, 0xfff4c000
	s_lshl_b32 s41, s83, 8
	s_lshl_b32 s42, s80, 4
	s_lshl_b32 s43, s83, 7
	s_mov_b32 s91, 0
	s_mov_b32 s44, 0xc3e00000
	s_movk_i32 s45, 0x7fff
	s_mov_b32 s46, 0xffff0000
	s_movk_i32 s47, 0x2c2f
	s_movk_i32 s48, 0x2c50
	s_mov_b32 s49, 0xb140
	v_add_u32_e32 v61, 0x400, v19
	v_add_u32_e32 v62, 0x800, v19
	v_add_u32_e32 v63, 0xc00, v19
	v_mov_b32_e32 v64, 0x43e00000
	s_mov_b32 s50, s80
	s_mov_b32 s13, -1
	s_mov_b32 s15, -1
	s_mov_b32 s19, -1
	s_mov_b32 s79, -1
	s_mov_b32 s93, -1
	s_mov_b32 s29, -1
	s_mov_b32 s35, -1
	s_mov_b32 s53, -1
	s_mov_b32 s55, -1
	s_mov_b32 s57, -1
	v_readlane_b32 s16, v253, 39
	v_readlane_b32 s17, v253, 40
	v_readlane_b32 s4, v253, 23
	v_readlane_b32 s5, v253, 24
	v_readlane_b32 s6, v253, 25
	v_readlane_b32 s7, v253, 26
	v_readlane_b32 s51, v253, 14
	s_branch .LBB0_15

; __global__ void __launch_bounds__(NWAVES * 64, 2) hybrid_fwd(Args args) {
;     ...
;         for (int it = gw; it < DEPTH * I_L; it += NGW) {
;             const int l = it / I_L; int r = it % I_L;
;             if (r < I_IN) { if (l >= PROJ_F8_FROM) p0_transpose_item_f8<true, 1>(args.in[2] + (size_t)l * DM * NSRC, DM, NSRC, NPROJ / 32, (unsigned char*)(ws + WS_WIN + l * SZ_WIN), WUP8_SCALE, args.in[1] + l * DM, args.in[1] + l * DM, DM, scr, r, lane);
;                 else p0_transpose_item<1, true>(args.in[2] + (size_t)l * DM * NSRC, DM, NSRC, NPROJ / 32, (bf16*)(ws + WS_WIN + l * SZ_WIN), args.in[1] + l * DM, args.in[1] + l * DM, DM, scr, r, lane); continue; } r -= I_IN;
;             if (r < I_O) { if (l >= WO_F8_FROM) p0_transpose_item_f8<true>(args.in[13] + (size_t)l * DM * DM, DM, DM, DM / 32, (unsigned char*)(ws + WS_WO + l * SZ_WO), 64.f, args.in[6] + l * 2048, args.in[12] + l * 2048, 2048, scr, r, lane);
;                 else p0_transpose_item<0, true>(args.in[13] + (size_t)l * DM * DM, DM, DM, DM / 32, (bf16*)(ws + WS_WO + l * SZ_WO), args.in[6] + l * 2048, args.in[12] + l * 2048, 2048, scr, r, lane); continue; } r -= I_O;
;             if (r < I_UP) { p0_transpose_item_f8<true>(args.in[15] + (size_t)l * DM * FF, DM, FF, FF / 32, (unsigned char*)(ws + WS_WUP + l * SZ_WUP), WUP8_SCALE, args.in[14] + l * DM, args.in[14] + l * DM, DM, scr, r, lane); continue; } r -= I_UP;
;             p0_transpose_item_f8<false>(args.in[16] + (size_t)l * FF * DM, FF, DM, DM / 32, (unsigned char*)(ws + WS_WDN + l * SZ_WDN), 128.f, args.in[16], args.in[16], 0, scr, r, lane);
.LBB0_15:
	s_mul_hi_i32 s0, s50, 0xad602b59
	s_add_i32 s0, s0, s50
	s_lshr_b32 s1, s0, 31
	s_ashr_i32 s0, s0, 16
	s_add_i32 s58, s0, s1
	s_mul_i32 s0, s58, 0xfffe8600
	s_add_i32 s51, s50, s0
	s_cmpk_gt_i32 s51, 0x59ff
	s_mov_b64 s[0:1], -1
	s_cbranch_scc0 .LBB0_28
	s_cmpk_gt_u32 s51, 0x79ff
	s_cbranch_scc0 .LBB0_22
	s_branch .LBB0_14
